# baseline (speedup 1.0000x reference)
_Z5k_fftPKtPtPKDv2_f:
	s_load_dwordx2 s[6:7], s[0:1], 0x10
	s_load_dwordx2 s[8:9], s[0:1], 0x0
	v_and_b32_e32 v1, 0xf0, v0
	v_and_b32_e32 v18, 15, v0
	v_mul_u32_u24_e32 v1, v1, v18
	v_lshlrev_b32_e32 v1, 3, v1
	s_waitcnt lgkmcnt(0)
	global_load_dwordx2 v[86:87], v1, s[6:7]
	s_lshr_b32 s4, s2, 3
	s_and_b32 s3, s2, 7
	s_and_b32 s4, s4, 0x1ffffff8
	s_or_b32 s4, s4, s3
	s_bfe_u32 s16, s2, 0x30003
	s_lshl_b32 s3, s4, 3
	s_or_b32 s3, s3, s16
	s_lshl_b32 s22, s3, 14
	s_add_u32 s22, s8, s22
	s_addc_u32 s23, s9, 0
	s_mov_b32 s11, 0
	s_lshr_b32 s10, s3, 1
	s_lshl_b64 s[10:11], s[10:11], 14
	s_add_u32 s3, s8, s10
	s_addc_u32 s8, s9, s11
	s_lshr_b32 s2, s2, 2
	s_and_b32 s2, s2, 2
	s_add_u32 s2, s3, s2
	v_mov_b32_e32 v3, 0
	v_lshlrev_b32_e32 v2, 2, v0
	s_addc_u32 s3, s8, 0
	s_movk_i32 s5, 0x1000
	v_lshl_add_u64 v[6:7], s[2:3], 0, v[2:3]
	v_add_co_u32_e32 v8, vcc, s5, v6
	s_movk_i32 s12, 0x2000
	s_nop 0
	v_addc_co_u32_e32 v9, vcc, 0, v7, vcc
	v_add_co_u32_e32 v10, vcc, s12, v6
	s_movk_i32 s13, 0x3000
	s_add_u32 s8, s2, 0x1000000
	v_addc_co_u32_e32 v11, vcc, 0, v7, vcc
	s_addc_u32 s9, s3, 0
	s_add_u32 s20, s2, 0x2000000
	s_addc_u32 s21, s3, 0
	v_add_co_u32_e32 v6, vcc, s13, v6
	v_lshl_add_u64 v[12:13], s[8:9], 0, v[2:3]
	s_nop 0
	v_addc_co_u32_e32 v7, vcc, 0, v7, vcc
	v_add_co_u32_e32 v14, vcc, s5, v12
	v_lshlrev_b32_e32 v1, 3, v0
	s_nop 0
	v_addc_co_u32_e32 v15, vcc, 0, v13, vcc
	v_add_co_u32_e32 v16, vcc, s12, v12
	v_or_b32_e32 v19, 0x1000, v2
	s_nop 0
	v_addc_co_u32_e32 v17, vcc, 0, v13, vcc
	v_add_co_u32_e32 v12, vcc, s13, v12
	v_or_b32_e32 v20, 0x2000, v2
	v_or_b32_e32 v21, 0x3000, v2
	v_addc_co_u32_e32 v13, vcc, 0, v13, vcc
	v_mul_u32_u24_e32 v3, 3, v0
	s_movk_i32 s5, 0x888
	v_lshlrev_b32_e32 v3, 3, v3
	s_mov_b32 s10, 0x3ec3ef15
	s_mov_b32 s11, 0xbf6c835e
	s_mov_b32 s14, s11
	s_mov_b32 s15, s10
	s_mov_b32 s12, 0xbf3504f3
	s_mov_b32 s13, s12
	v_mov_b32_e32 v88, v0
	global_load_dword v85, v2, s[22:23] nt
	global_load_dword v84, v2, s[22:23] offset:1024 nt
	global_load_dword v83, v2, s[22:23] offset:2048 nt
	global_load_dword v82, v2, s[22:23] offset:3072 nt
	global_load_dword v81, v19, s[22:23] nt
	global_load_dword v80, v19, s[22:23] offset:1024 nt
	global_load_dword v79, v19, s[22:23] offset:2048 nt
	global_load_dword v78, v19, s[22:23] offset:3072 nt
	global_load_dword v77, v20, s[22:23] nt
	global_load_dword v76, v20, s[22:23] offset:1024 nt
	global_load_dword v75, v20, s[22:23] offset:2048 nt
	global_load_dword v74, v20, s[22:23] offset:3072 nt
	global_load_dword v73, v21, s[22:23] nt
	global_load_dword v72, v21, s[22:23] offset:1024 nt
	global_load_dword v71, v21, s[22:23] offset:2048 nt
	global_load_dword v70, v21, s[22:23] offset:3072 nt
	v_mul_u32_u24_e32 v5, 5, v0
	v_mul_u32_u24_e32 v6, 6, v0
	v_mul_u32_u24_e32 v7, 7, v0
	v_mul_u32_u24_e32 v9, 9, v0
	v_mul_u32_u24_e32 v10, 10, v0
	v_lshrrev_b32_e32 v16, 1, v0
	v_lshlrev_b32_e32 v2, 4, v0
	v_lshlrev_b32_e32 v4, 5, v0
	v_lshlrev_b32_e32 v8, 6, v0
	v_mul_u32_u24_e32 v11, 11, v0
	v_mul_u32_u24_e32 v12, 12, v0
	v_mul_u32_u24_e32 v13, 13, v0
	v_mul_u32_u24_e32 v14, 14, v0
	v_mul_u32_u24_e32 v15, 15, v0
	v_lshlrev_b32_e32 v5, 3, v5
	v_lshlrev_b32_e32 v6, 3, v6
	v_lshlrev_b32_e32 v7, 3, v7
	v_lshlrev_b32_e32 v9, 3, v9
	v_lshlrev_b32_e32 v64, 3, v10
	v_and_b32_e32 v10, 0x78, v16
	v_lshlrev_b32_e32 v65, 3, v11
	v_lshlrev_b32_e32 v66, 3, v12
	v_lshlrev_b32_e32 v67, 3, v13
	v_lshlrev_b32_e32 v68, 3, v14
	v_lshlrev_b32_e32 v69, 3, v15
	v_mad_u32_u24 v96, v18, s5, v10
	global_load_dwordx2 v[30:31], v1, s[6:7]
	s_nop 0
	s_mov_b32 s6, 0x3f6c835e
	s_mov_b32 s7, 0xbec3ef15
	s_mov_b32 s8, 0x3f3504f3
	s_mov_b32 s9, s8
	s_waitcnt vmcnt(16)
	v_cvt_f32_fp8_e32 v32, v85
	s_waitcnt vmcnt(15)
	v_cvt_f32_fp8_sdwa v33, v85 src0_sel:BYTE_2
	s_waitcnt vmcnt(14)
	v_cvt_f32_fp8_e32 v34, v84
	v_cvt_f32_fp8_sdwa v35, v84 src0_sel:BYTE_2
	s_waitcnt vmcnt(13)
	s_waitcnt vmcnt(12)
	v_cvt_f32_fp8_e32 v40, v81
	s_waitcnt vmcnt(11)
	v_cvt_f32_fp8_sdwa v41, v81 src0_sel:BYTE_2
	s_waitcnt vmcnt(10)
	v_cvt_f32_fp8_e32 v42, v80
	v_cvt_f32_fp8_sdwa v43, v80 src0_sel:BYTE_2
	v_cvt_f32_fp8_e32 v36, v83
	v_cvt_f32_fp8_sdwa v37, v83 src0_sel:BYTE_2
	s_waitcnt vmcnt(9)
	v_cvt_f32_fp8_e32 v44, v79
	s_waitcnt vmcnt(8)
	v_cvt_f32_fp8_e32 v48, v77
	s_waitcnt vmcnt(7)
	v_cvt_f32_fp8_sdwa v49, v77 src0_sel:BYTE_2
	s_waitcnt vmcnt(6)
	v_cvt_f32_fp8_e32 v50, v76
	v_cvt_f32_fp8_sdwa v51, v76 src0_sel:BYTE_2
	s_waitcnt vmcnt(5)
	s_waitcnt vmcnt(4)
	v_cvt_f32_fp8_e32 v56, v73
	s_waitcnt vmcnt(3)
	v_cvt_f32_fp8_sdwa v57, v73 src0_sel:BYTE_2
	s_waitcnt vmcnt(2)
	v_cvt_f32_fp8_e32 v58, v72
	v_cvt_f32_fp8_sdwa v59, v72 src0_sel:BYTE_2
	v_cvt_f32_fp8_sdwa v45, v79 src0_sel:BYTE_2
	v_cvt_f32_fp8_e32 v52, v75
	v_cvt_f32_fp8_sdwa v53, v75 src0_sel:BYTE_2
	v_cvt_f32_fp8_e32 v60, v71
	v_cvt_f32_fp8_sdwa v61, v71 src0_sel:BYTE_2
	s_waitcnt vmcnt(1)
	v_cvt_f32_fp8_e32 v38, v82
	v_cvt_f32_fp8_sdwa v39, v82 src0_sel:BYTE_2
	v_cvt_f32_fp8_e32 v46, v78
	v_cvt_f32_fp8_sdwa v47, v78 src0_sel:BYTE_2
	v_cvt_f32_fp8_e32 v54, v74
	v_cvt_f32_fp8_sdwa v55, v74 src0_sel:BYTE_2
	v_cvt_f32_fp8_e32 v62, v70
	v_cvt_f32_fp8_sdwa v63, v70 src0_sel:BYTE_2
	v_pk_add_f32 v[64:65], v[32:33], v[48:49]
	v_pk_add_f32 v[32:33], v[32:33], v[48:49] neg_lo:[0,1] neg_hi:[0,1]
	v_pk_add_f32 v[48:49], v[40:41], v[56:57]
	v_pk_add_f32 v[40:41], v[40:41], v[56:57] neg_lo:[0,1] neg_hi:[0,1]
	v_pk_add_f32 v[56:57], v[64:65], v[48:49]
	v_pk_add_f32 v[48:49], v[64:65], v[48:49] neg_lo:[0,1] neg_hi:[0,1]
	v_pk_add_f32 v[64:65], v[32:33], v[40:41] op_sel:[0,1] op_sel_hi:[1,0] neg_hi:[0,1]
	v_pk_add_f32 v[32:33], v[32:33], v[40:41] op_sel:[0,1] op_sel_hi:[1,0] neg_lo:[0,1]
	v_pk_add_f32 v[40:41], v[34:35], v[50:51]
	v_pk_add_f32 v[34:35], v[34:35], v[50:51] neg_lo:[0,1] neg_hi:[0,1]
	v_pk_add_f32 v[50:51], v[42:43], v[58:59]
	v_pk_add_f32 v[42:43], v[42:43], v[58:59] neg_lo:[0,1] neg_hi:[0,1]
	v_pk_add_f32 v[58:59], v[40:41], v[50:51]
	v_pk_add_f32 v[40:41], v[40:41], v[50:51] neg_lo:[0,1] neg_hi:[0,1]
	v_pk_add_f32 v[50:51], v[34:35], v[42:43] op_sel:[0,1] op_sel_hi:[1,0] neg_hi:[0,1]
	v_pk_add_f32 v[34:35], v[34:35], v[42:43] op_sel:[0,1] op_sel_hi:[1,0] neg_lo:[0,1]
	v_pk_add_f32 v[42:43], v[36:37], v[52:53]
	v_pk_add_f32 v[36:37], v[36:37], v[52:53] neg_lo:[0,1] neg_hi:[0,1]
	v_pk_add_f32 v[52:53], v[44:45], v[60:61]
	v_pk_add_f32 v[44:45], v[44:45], v[60:61] neg_lo:[0,1] neg_hi:[0,1]
	v_pk_add_f32 v[60:61], v[42:43], v[52:53]
	v_pk_add_f32 v[42:43], v[42:43], v[52:53] neg_lo:[0,1] neg_hi:[0,1]
	v_pk_add_f32 v[52:53], v[36:37], v[44:45] op_sel:[0,1] op_sel_hi:[1,0] neg_hi:[0,1]
	v_pk_add_f32 v[36:37], v[36:37], v[44:45] op_sel:[0,1] op_sel_hi:[1,0] neg_lo:[0,1]
	v_pk_add_f32 v[44:45], v[38:39], v[54:55]
	v_pk_add_f32 v[38:39], v[38:39], v[54:55] neg_lo:[0,1] neg_hi:[0,1]
	v_pk_add_f32 v[54:55], v[46:47], v[62:63]
	v_pk_add_f32 v[46:47], v[46:47], v[62:63] neg_lo:[0,1] neg_hi:[0,1]
	v_pk_add_f32 v[62:63], v[44:45], v[54:55]
	v_pk_add_f32 v[44:45], v[44:45], v[54:55] neg_lo:[0,1] neg_hi:[0,1]
	v_pk_add_f32 v[54:55], v[38:39], v[46:47] op_sel:[0,1] op_sel_hi:[1,0] neg_hi:[0,1]
	v_pk_add_f32 v[38:39], v[38:39], v[46:47] op_sel:[0,1] op_sel_hi:[1,0] neg_lo:[0,1]
	v_pk_mul_f32 v[46:47], v[50:51], s[6:7] op_sel:[0,0] op_sel_hi:[0,1]
	v_pk_fma_f32 v[46:47], v[50:51], s[6:7], v[46:47] op_sel:[1,1,0] op_sel_hi:[1,0,1] neg_lo:[0,1,0]
	v_pk_mul_f32 v[50:51], v[34:35], s[10:11] op_sel:[0,0] op_sel_hi:[0,1]
	v_pk_fma_f32 v[50:51], v[34:35], s[10:11], v[50:51] op_sel:[1,1,0] op_sel_hi:[1,0,1] neg_lo:[0,1,0]
	v_pk_add_f32 v[34:35], v[52:53], v[52:53] op_sel:[0,1] op_sel_hi:[1,0] neg_hi:[0,1]
	v_pk_add_f32 v[40:41], v[40:41], v[40:41] op_sel:[0,1] op_sel_hi:[1,0] neg_hi:[0,1]
	s_nop 0
	v_pk_mul_f32 v[52:53], v[54:55], s[10:11] op_sel:[0,0] op_sel_hi:[0,1]
	v_pk_fma_f32 v[52:53], v[54:55], s[10:11], v[52:53] op_sel:[1,1,0] op_sel_hi:[1,0,1] neg_lo:[0,1,0]
	v_pk_mul_f32 v[54:55], v[38:39], s[14:15] op_sel:[0,0] op_sel_hi:[0,1]
	v_pk_fma_f32 v[54:55], v[38:39], s[14:15], v[54:55] op_sel:[1,1,0] op_sel_hi:[1,0,1] neg_lo:[0,1,0]
	v_pk_add_f32 v[38:39], v[56:57], v[60:61]
	v_pk_mul_f32 v[34:35], v[34:35], s[8:9]
	v_pk_add_f32 v[56:57], v[56:57], v[60:61] neg_lo:[0,1] neg_hi:[0,1]
	v_pk_add_f32 v[60:61], v[58:59], v[62:63]
	v_pk_add_f32 v[58:59], v[58:59], v[62:63] neg_lo:[0,1] neg_hi:[0,1]
	v_pk_mul_f32 v[40:41], v[40:41], s[8:9]
	v_pk_add_f32 v[36:37], v[36:37], v[36:37] op_sel:[0,1] op_sel_hi:[1,0] neg_lo:[0,1]
	v_pk_add_f32 v[44:45], v[44:45], v[44:45] op_sel:[0,1] op_sel_hi:[1,0] neg_lo:[0,1]
	v_pk_add_f32 v[62:63], v[38:39], v[60:61]
	v_pk_add_f32 v[38:39], v[38:39], v[60:61] neg_lo:[0,1] neg_hi:[0,1]
	v_pk_add_f32 v[60:61], v[56:57], v[58:59] op_sel:[0,1] op_sel_hi:[1,0] neg_hi:[0,1]
	v_pk_add_f32 v[56:57], v[56:57], v[58:59] op_sel:[0,1] op_sel_hi:[1,0] neg_lo:[0,1]
	v_pk_add_f32 v[58:59], v[64:65], v[34:35]
	v_pk_add_f32 v[34:35], v[64:65], v[34:35] neg_lo:[0,1] neg_hi:[0,1]
	v_pk_add_f32 v[64:65], v[46:47], v[52:53]
	v_pk_add_f32 v[46:47], v[46:47], v[52:53] neg_lo:[0,1] neg_hi:[0,1]
	v_pk_mul_f32 v[36:37], v[36:37], s[12:13]
	v_pk_mul_f32 v[44:45], v[44:45], s[12:13]
	v_pk_add_f32 v[52:53], v[58:59], v[64:65]
	v_pk_add_f32 v[58:59], v[58:59], v[64:65] neg_lo:[0,1] neg_hi:[0,1]
	v_pk_add_f32 v[64:65], v[34:35], v[46:47] op_sel:[0,1] op_sel_hi:[1,0] neg_hi:[0,1]
	v_pk_add_f32 v[34:35], v[34:35], v[46:47] op_sel:[0,1] op_sel_hi:[1,0] neg_lo:[0,1]
	v_pk_add_f32 v[46:47], v[48:49], v[42:43] op_sel:[0,1] op_sel_hi:[1,0] neg_hi:[0,1]
	v_pk_add_f32 v[42:43], v[48:49], v[42:43] op_sel:[0,1] op_sel_hi:[1,0] neg_lo:[0,1]
	v_pk_add_f32 v[48:49], v[40:41], v[44:45]
	v_pk_add_f32 v[40:41], v[40:41], v[44:45] neg_lo:[0,1] neg_hi:[0,1]
	v_pk_add_f32 v[44:45], v[48:49], v[46:47]
	v_pk_add_f32 v[46:47], v[46:47], v[48:49] neg_lo:[0,1] neg_hi:[0,1]
	v_pk_add_f32 v[48:49], v[42:43], v[40:41] op_sel:[0,1] op_sel_hi:[1,0] neg_hi:[0,1]
	v_pk_add_f32 v[40:41], v[42:43], v[40:41] op_sel:[0,1] op_sel_hi:[1,0] neg_lo:[0,1]
	v_pk_add_f32 v[42:43], v[32:33], v[36:37]
	v_pk_add_f32 v[32:33], v[32:33], v[36:37] neg_lo:[0,1] neg_hi:[0,1]
	v_pk_add_f32 v[36:37], v[50:51], v[54:55]
	v_pk_add_f32 v[50:51], v[50:51], v[54:55] neg_lo:[0,1] neg_hi:[0,1]
	v_pk_add_f32 v[54:55], v[42:43], v[36:37]
	v_pk_add_f32 v[36:37], v[42:43], v[36:37] neg_lo:[0,1] neg_hi:[0,1]
	v_pk_add_f32 v[42:43], v[32:33], v[50:51] op_sel:[0,1] op_sel_hi:[1,0] neg_hi:[0,1]
	v_pk_add_f32 v[32:33], v[32:33], v[50:51] op_sel:[0,1] op_sel_hi:[1,0] neg_lo:[0,1]
	s_waitcnt vmcnt(0)
	v_pk_mul_f32 v[28:29], v[30:31], v[30:31] op_sel:[0,0] op_sel_hi:[0,1]
	v_pk_fma_f32 v[28:29], v[30:31], v[30:31], v[28:29] op_sel:[1,1,0] op_sel_hi:[1,0,1] neg_lo:[0,1,0]
	v_pk_mul_f32 v[24:25], v[28:29], v[28:29] op_sel:[0,0] op_sel_hi:[0,1]
	v_pk_fma_f32 v[24:25], v[28:29], v[28:29], v[24:25] op_sel:[1,1,0] op_sel_hi:[1,0,1] neg_lo:[0,1,0]
	v_pk_mul_f32 v[22:23], v[24:25], v[24:25] op_sel:[0,0] op_sel_hi:[0,1]
	v_pk_fma_f32 v[22:23], v[24:25], v[24:25], v[22:23] op_sel:[1,1,0] op_sel_hi:[1,0,1] neg_lo:[0,1,0]
	v_pk_mul_f32 v[26:27], v[30:31], v[28:29] op_sel:[0,0] op_sel_hi:[0,1]
	v_pk_fma_f32 v[26:27], v[30:31], v[28:29], v[26:27] op_sel:[1,1,0] op_sel_hi:[1,0,1] neg_lo:[0,1,0]
	v_pk_mul_f32 v[20:21], v[30:31], v[24:25] op_sel:[0,0] op_sel_hi:[0,1]
	v_pk_fma_f32 v[20:21], v[30:31], v[24:25], v[20:21] op_sel:[1,1,0] op_sel_hi:[1,0,1] neg_lo:[0,1,0]
	v_pk_mul_f32 v[16:17], v[28:29], v[24:25] op_sel:[0,0] op_sel_hi:[0,1]
	v_pk_fma_f32 v[16:17], v[28:29], v[24:25], v[16:17] op_sel:[1,1,0] op_sel_hi:[1,0,1] neg_lo:[0,1,0]
	v_pk_mul_f32 v[18:19], v[30:31], v[22:23] op_sel:[0,0] op_sel_hi:[0,1]
	v_pk_fma_f32 v[18:19], v[30:31], v[22:23], v[18:19] op_sel:[1,1,0] op_sel_hi:[1,0,1] neg_lo:[0,1,0]
	v_pk_mul_f32 v[12:13], v[28:29], v[22:23] op_sel:[0,0] op_sel_hi:[0,1]
	v_pk_fma_f32 v[12:13], v[28:29], v[22:23], v[12:13] op_sel:[1,1,0] op_sel_hi:[1,0,1] neg_lo:[0,1,0]
	v_pk_mul_f32 v[6:7], v[24:25], v[22:23] op_sel:[0,0] op_sel_hi:[0,1]
	v_pk_fma_f32 v[6:7], v[24:25], v[22:23], v[6:7] op_sel:[1,1,0] op_sel_hi:[1,0,1] neg_lo:[0,1,0]
	v_pk_mul_f32 v[10:11], v[26:27], v[24:25] op_sel:[0,0] op_sel_hi:[0,1]
	v_pk_fma_f32 v[10:11], v[26:27], v[24:25], v[10:11] op_sel:[1,1,0] op_sel_hi:[1,0,1] neg_lo:[0,1,0]
	v_pk_mul_f32 v[14:15], v[26:27], v[22:23] op_sel:[0,0] op_sel_hi:[0,1]
	v_pk_fma_f32 v[14:15], v[26:27], v[22:23], v[14:15] op_sel:[1,1,0] op_sel_hi:[1,0,1] neg_lo:[0,1,0]
	v_pk_mul_f32 v[8:9], v[20:21], v[22:23] op_sel:[0,0] op_sel_hi:[0,1]
	v_pk_fma_f32 v[8:9], v[20:21], v[22:23], v[8:9] op_sel:[1,1,0] op_sel_hi:[1,0,1] neg_lo:[0,1,0]
	v_pk_mul_f32 v[4:5], v[16:17], v[22:23] op_sel:[0,0] op_sel_hi:[0,1]
	v_pk_fma_f32 v[4:5], v[16:17], v[22:23], v[4:5] op_sel:[1,1,0] op_sel_hi:[1,0,1] neg_lo:[0,1,0]
	v_pk_mul_f32 v[2:3], v[10:11], v[22:23] op_sel:[0,0] op_sel_hi:[0,1]
	v_pk_fma_f32 v[2:3], v[10:11], v[22:23], v[2:3] op_sel:[1,1,0] op_sel_hi:[1,0,1] neg_lo:[0,1,0]
	v_pk_mul_f32 v[50:51], v[52:53], v[30:31] op_sel:[0,0] op_sel_hi:[0,1]
	v_pk_fma_f32 v[50:51], v[52:53], v[30:31], v[50:51] op_sel:[1,1,0] op_sel_hi:[1,0,1] neg_lo:[0,1,0]
	ds_write_b64 v1, v[50:51] offset:2184
	v_pk_mul_f32 v[50:51], v[44:45], v[28:29] op_sel:[0,0] op_sel_hi:[0,1]
	v_pk_fma_f32 v[50:51], v[44:45], v[28:29], v[50:51] op_sel:[1,1,0] op_sel_hi:[1,0,1] neg_lo:[0,1,0]
	v_pk_mul_f32 v[44:45], v[54:55], v[26:27] op_sel:[0,0] op_sel_hi:[0,1]
	v_pk_fma_f32 v[44:45], v[54:55], v[26:27], v[44:45] op_sel:[1,1,0] op_sel_hi:[1,0,1] neg_lo:[0,1,0]
	ds_write_b64 v1, v[44:45] offset:6552
	v_pk_mul_f32 v[44:45], v[60:61], v[24:25] op_sel:[0,0] op_sel_hi:[0,1]
	v_pk_fma_f32 v[44:45], v[60:61], v[24:25], v[44:45] op_sel:[1,1,0] op_sel_hi:[1,0,1] neg_lo:[0,1,0]
	ds_write_b64 v1, v[44:45] offset:8736
	v_pk_mul_f32 v[44:45], v[64:65], v[20:21] op_sel:[0,0] op_sel_hi:[0,1]
	v_pk_fma_f32 v[44:45], v[64:65], v[20:21], v[44:45] op_sel:[1,1,0] op_sel_hi:[1,0,1] neg_lo:[0,1,0]
	ds_write_b64 v1, v[44:45] offset:10920
	v_pk_mul_f32 v[44:45], v[48:49], v[16:17] op_sel:[0,0] op_sel_hi:[0,1]
	v_pk_fma_f32 v[44:45], v[48:49], v[16:17], v[44:45] op_sel:[1,1,0] op_sel_hi:[1,0,1] neg_lo:[0,1,0]
	ds_write_b64 v1, v[44:45] offset:13104
	v_pk_mul_f32 v[44:45], v[42:43], v[10:11] op_sel:[0,0] op_sel_hi:[0,1]
	v_pk_fma_f32 v[44:45], v[42:43], v[10:11], v[44:45] op_sel:[1,1,0] op_sel_hi:[1,0,1] neg_lo:[0,1,0]
	v_pk_mul_f32 v[42:43], v[38:39], v[22:23] op_sel:[0,0] op_sel_hi:[0,1]
	v_pk_fma_f32 v[42:43], v[38:39], v[22:23], v[42:43] op_sel:[1,1,0] op_sel_hi:[1,0,1] neg_lo:[0,1,0]
	v_pk_mul_f32 v[38:39], v[58:59], v[18:19] op_sel:[0,0] op_sel_hi:[0,1]
	v_pk_fma_f32 v[38:39], v[58:59], v[18:19], v[38:39] op_sel:[1,1,0] op_sel_hi:[1,0,1] neg_lo:[0,1,0]
	ds_write_b64 v1, v[38:39] offset:19656
	v_pk_mul_f32 v[38:39], v[46:47], v[12:13] op_sel:[0,0] op_sel_hi:[0,1]
	v_pk_fma_f32 v[38:39], v[46:47], v[12:13], v[38:39] op_sel:[1,1,0] op_sel_hi:[1,0,1] neg_lo:[0,1,0]
	ds_write_b64 v1, v[38:39] offset:21840
	v_pk_mul_f32 v[38:39], v[36:37], v[14:15] op_sel:[0,0] op_sel_hi:[0,1]
	v_pk_fma_f32 v[38:39], v[36:37], v[14:15], v[38:39] op_sel:[1,1,0] op_sel_hi:[1,0,1] neg_lo:[0,1,0]
	v_pk_mul_f32 v[36:37], v[56:57], v[6:7] op_sel:[0,0] op_sel_hi:[0,1]
	v_pk_fma_f32 v[36:37], v[56:57], v[6:7], v[36:37] op_sel:[1,1,0] op_sel_hi:[1,0,1] neg_lo:[0,1,0]
	ds_write_b64 v1, v[36:37] offset:26208
	v_pk_mul_f32 v[36:37], v[34:35], v[8:9] op_sel:[0,0] op_sel_hi:[0,1]
	v_pk_fma_f32 v[36:37], v[34:35], v[8:9], v[36:37] op_sel:[1,1,0] op_sel_hi:[1,0,1] neg_lo:[0,1,0]
	v_pk_mul_f32 v[34:35], v[40:41], v[4:5] op_sel:[0,0] op_sel_hi:[0,1]
	v_pk_fma_f32 v[34:35], v[40:41], v[4:5], v[34:35] op_sel:[1,1,0] op_sel_hi:[1,0,1] neg_lo:[0,1,0]
	ds_write_b64 v1, v[34:35] offset:30576
	v_pk_mul_f32 v[34:35], v[32:33], v[2:3] op_sel:[0,0] op_sel_hi:[0,1]
	v_pk_fma_f32 v[34:35], v[32:33], v[2:3], v[34:35] op_sel:[1,1,0] op_sel_hi:[1,0,1] neg_lo:[0,1,0]
	ds_write_b64 v1, v[62:63]
	ds_write_b64 v1, v[50:51] offset:4368
	ds_write_b64 v1, v[44:45] offset:15288
	ds_write_b64 v1, v[42:43] offset:17472
	ds_write_b64 v1, v[38:39] offset:24024
	ds_write_b64 v1, v[36:37] offset:28392
	ds_write_b64 v1, v[34:35] offset:32760
	ds_write_b64 v1, v[86:87] offset:34816
	s_waitcnt lgkmcnt(0)
	s_barrier
	ds_read2_b64 v[32:35], v96 offset1:16
	ds_read2_b64 v[36:39], v96 offset0:32 offset1:48
	ds_read2_b64 v[40:43], v96 offset0:64 offset1:80
	ds_read2_b64 v[44:47], v96 offset0:128 offset1:144
	ds_read2_b64 v[48:51], v96 offset0:96 offset1:112
	ds_read2_b64 v[52:55], v96 offset0:192 offset1:208
	ds_read2_b64 v[56:59], v96 offset0:160 offset1:176
	ds_read2_b64 v[60:63], v96 offset0:224 offset1:240
	v_lshlrev_b32_e32 v115, 2, v0
	v_lshlrev_b32_e32 v119, 2, v0
	v_lshlrev_b32_e32 v123, 2, v0
	v_lshlrev_b32_e32 v127, 2, v0
	v_or_b32_e32 v119, 0x1000, v119
	v_or_b32_e32 v123, 0x2000, v123
	v_or_b32_e32 v127, 0x3000, v127
	global_load_ushort v112, v115, s[20:21]
	global_load_ushort v113, v115, s[20:21] offset:1024
	global_load_ushort v114, v115, s[20:21] offset:2048
	global_load_ushort v115, v115, s[20:21] offset:3072
	global_load_ushort v116, v119, s[20:21]
	global_load_ushort v117, v119, s[20:21] offset:1024
	global_load_ushort v118, v119, s[20:21] offset:2048
	global_load_ushort v119, v119, s[20:21] offset:3072
	global_load_ushort v120, v123, s[20:21]
	global_load_ushort v121, v123, s[20:21] offset:1024
	global_load_ushort v122, v123, s[20:21] offset:2048
	global_load_ushort v123, v123, s[20:21] offset:3072
	global_load_ushort v124, v127, s[20:21]
	global_load_ushort v125, v127, s[20:21] offset:1024
	global_load_ushort v126, v127, s[20:21] offset:2048
	global_load_ushort v127, v127, s[20:21] offset:3072
	s_waitcnt lgkmcnt(4)
	v_pk_add_f32 v[64:65], v[32:33], v[44:45]
	v_pk_add_f32 v[32:33], v[32:33], v[44:45] neg_lo:[0,1] neg_hi:[0,1]
	s_waitcnt lgkmcnt(2)
	v_pk_add_f32 v[44:45], v[40:41], v[52:53]
	v_pk_add_f32 v[40:41], v[40:41], v[52:53] neg_lo:[0,1] neg_hi:[0,1]
	v_pk_add_f32 v[52:53], v[64:65], v[44:45]
	v_pk_add_f32 v[44:45], v[64:65], v[44:45] neg_lo:[0,1] neg_hi:[0,1]
	v_pk_add_f32 v[64:65], v[32:33], v[40:41] op_sel:[0,1] op_sel_hi:[1,0] neg_hi:[0,1]
	v_pk_add_f32 v[32:33], v[32:33], v[40:41] op_sel:[0,1] op_sel_hi:[1,0] neg_lo:[0,1]
	v_pk_add_f32 v[40:41], v[34:35], v[46:47]
	v_pk_add_f32 v[34:35], v[34:35], v[46:47] neg_lo:[0,1] neg_hi:[0,1]
	v_pk_add_f32 v[46:47], v[42:43], v[54:55]
	v_pk_add_f32 v[42:43], v[42:43], v[54:55] neg_lo:[0,1] neg_hi:[0,1]
	v_pk_add_f32 v[54:55], v[40:41], v[46:47]
	v_pk_add_f32 v[40:41], v[40:41], v[46:47] neg_lo:[0,1] neg_hi:[0,1]
	v_pk_add_f32 v[46:47], v[34:35], v[42:43] op_sel:[0,1] op_sel_hi:[1,0] neg_hi:[0,1]
	v_pk_add_f32 v[34:35], v[34:35], v[42:43] op_sel:[0,1] op_sel_hi:[1,0] neg_lo:[0,1]
	s_waitcnt lgkmcnt(1)
	v_pk_add_f32 v[42:43], v[36:37], v[56:57]
	v_pk_add_f32 v[36:37], v[36:37], v[56:57] neg_lo:[0,1] neg_hi:[0,1]
	s_waitcnt lgkmcnt(0)
	v_pk_add_f32 v[56:57], v[48:49], v[60:61]
	v_pk_add_f32 v[48:49], v[48:49], v[60:61] neg_lo:[0,1] neg_hi:[0,1]
	v_pk_add_f32 v[60:61], v[42:43], v[56:57]
	v_pk_add_f32 v[42:43], v[42:43], v[56:57] neg_lo:[0,1] neg_hi:[0,1]
	v_pk_add_f32 v[56:57], v[36:37], v[48:49] op_sel:[0,1] op_sel_hi:[1,0] neg_hi:[0,1]
	v_pk_add_f32 v[36:37], v[36:37], v[48:49] op_sel:[0,1] op_sel_hi:[1,0] neg_lo:[0,1]
	v_pk_add_f32 v[48:49], v[38:39], v[58:59]
	v_pk_add_f32 v[38:39], v[38:39], v[58:59] neg_lo:[0,1] neg_hi:[0,1]
	v_pk_add_f32 v[58:59], v[50:51], v[62:63]
	v_pk_add_f32 v[50:51], v[50:51], v[62:63] neg_lo:[0,1] neg_hi:[0,1]
	v_pk_add_f32 v[62:63], v[48:49], v[58:59]
	v_pk_add_f32 v[48:49], v[48:49], v[58:59] neg_lo:[0,1] neg_hi:[0,1]
	v_pk_add_f32 v[58:59], v[38:39], v[50:51] op_sel:[0,1] op_sel_hi:[1,0] neg_hi:[0,1]
	v_pk_add_f32 v[38:39], v[38:39], v[50:51] op_sel:[0,1] op_sel_hi:[1,0] neg_lo:[0,1]
	v_pk_mul_f32 v[50:51], v[46:47], s[6:7] op_sel:[0,0] op_sel_hi:[0,1]
	v_pk_fma_f32 v[50:51], v[46:47], s[6:7], v[50:51] op_sel:[1,1,0] op_sel_hi:[1,0,1] neg_lo:[0,1,0]
	v_pk_mul_f32 v[46:47], v[34:35], s[10:11] op_sel:[0,0] op_sel_hi:[0,1]
	v_pk_fma_f32 v[46:47], v[34:35], s[10:11], v[46:47] op_sel:[1,1,0] op_sel_hi:[1,0,1] neg_lo:[0,1,0]
	v_pk_add_f32 v[34:35], v[56:57], v[56:57] op_sel:[0,1] op_sel_hi:[1,0] neg_hi:[0,1]
	v_pk_add_f32 v[40:41], v[40:41], v[40:41] op_sel:[0,1] op_sel_hi:[1,0] neg_hi:[0,1]
	s_nop 0
	v_pk_mul_f32 v[56:57], v[58:59], s[10:11] op_sel:[0,0] op_sel_hi:[0,1]
	v_pk_fma_f32 v[56:57], v[58:59], s[10:11], v[56:57] op_sel:[1,1,0] op_sel_hi:[1,0,1] neg_lo:[0,1,0]
	v_pk_mul_f32 v[58:59], v[38:39], s[14:15] op_sel:[0,0] op_sel_hi:[0,1]
	v_pk_fma_f32 v[58:59], v[38:39], s[14:15], v[58:59] op_sel:[1,1,0] op_sel_hi:[1,0,1] neg_lo:[0,1,0]
	v_pk_add_f32 v[38:39], v[52:53], v[60:61]
	v_pk_mul_f32 v[34:35], v[34:35], s[8:9]
	v_pk_add_f32 v[52:53], v[52:53], v[60:61] neg_lo:[0,1] neg_hi:[0,1]
	v_pk_add_f32 v[60:61], v[54:55], v[62:63]
	v_pk_add_f32 v[54:55], v[54:55], v[62:63] neg_lo:[0,1] neg_hi:[0,1]
	v_pk_add_f32 v[36:37], v[36:37], v[36:37] op_sel:[0,1] op_sel_hi:[1,0] neg_lo:[0,1]
	v_pk_add_f32 v[48:49], v[48:49], v[48:49] op_sel:[0,1] op_sel_hi:[1,0] neg_lo:[0,1]
	v_pk_add_f32 v[62:63], v[38:39], v[60:61]
	v_pk_add_f32 v[60:61], v[38:39], v[60:61] neg_lo:[0,1] neg_hi:[0,1]
	v_pk_add_f32 v[66:67], v[52:53], v[54:55] op_sel:[0,1] op_sel_hi:[1,0] neg_hi:[0,1]
	v_pk_add_f32 v[52:53], v[52:53], v[54:55] op_sel:[0,1] op_sel_hi:[1,0] neg_lo:[0,1]
	v_pk_add_f32 v[38:39], v[64:65], v[34:35]
	v_pk_add_f32 v[34:35], v[64:65], v[34:35] neg_lo:[0,1] neg_hi:[0,1]
	v_pk_add_f32 v[54:55], v[50:51], v[56:57]
	v_pk_add_f32 v[50:51], v[50:51], v[56:57] neg_lo:[0,1] neg_hi:[0,1]
	v_pk_mul_f32 v[40:41], v[40:41], s[8:9]
	v_pk_mul_f32 v[36:37], v[36:37], s[12:13]
	v_pk_mul_f32 v[48:49], v[48:49], s[12:13]
	v_pk_add_f32 v[56:57], v[38:39], v[54:55]
	v_pk_add_f32 v[54:55], v[38:39], v[54:55] neg_lo:[0,1] neg_hi:[0,1]
	v_pk_add_f32 v[64:65], v[34:35], v[50:51] op_sel:[0,1] op_sel_hi:[1,0] neg_hi:[0,1]
	v_pk_add_f32 v[50:51], v[34:35], v[50:51] op_sel:[0,1] op_sel_hi:[1,0] neg_lo:[0,1]
	v_pk_add_f32 v[34:35], v[44:45], v[42:43] op_sel:[0,1] op_sel_hi:[1,0] neg_hi:[0,1]
	v_pk_add_f32 v[38:39], v[44:45], v[42:43] op_sel:[0,1] op_sel_hi:[1,0] neg_lo:[0,1]
	v_pk_add_f32 v[42:43], v[40:41], v[48:49]
	v_pk_add_f32 v[40:41], v[40:41], v[48:49] neg_lo:[0,1] neg_hi:[0,1]
	v_pk_add_f32 v[44:45], v[42:43], v[34:35]
	v_pk_add_f32 v[42:43], v[34:35], v[42:43] neg_lo:[0,1] neg_hi:[0,1]
	v_pk_add_f32 v[34:35], v[32:33], v[36:37]
	v_pk_add_f32 v[36:37], v[32:33], v[36:37] neg_lo:[0,1] neg_hi:[0,1]
	v_pk_add_f32 v[32:33], v[46:47], v[58:59]
	v_pk_add_f32 v[48:49], v[38:39], v[40:41] op_sel:[0,1] op_sel_hi:[1,0] neg_hi:[0,1]
	v_pk_add_f32 v[40:41], v[38:39], v[40:41] op_sel:[0,1] op_sel_hi:[1,0] neg_lo:[0,1]
	v_pk_add_f32 v[38:39], v[46:47], v[58:59] neg_lo:[0,1] neg_hi:[0,1]
	v_pk_add_f32 v[46:47], v[34:35], v[32:33]
	v_pk_add_f32 v[58:59], v[34:35], v[32:33] neg_lo:[0,1] neg_hi:[0,1]
	v_pk_add_f32 v[68:69], v[36:37], v[38:39] op_sel:[0,1] op_sel_hi:[1,0] neg_hi:[0,1]
	v_pk_add_f32 v[86:87], v[36:37], v[38:39] op_sel:[0,1] op_sel_hi:[1,0] neg_lo:[0,1]
	s_nop 0
	v_ashrrev_i32_e32 v32, 4, v88
	v_lshlrev_b32_e32 v90, 3, v32
	v_add_u32_e32 v91, 0x8800, v90
	v_and_b32_e32 v36, 15, v88
	ds_read2_b64 v[32:35], v91 offset0:16 offset1:32
	v_mad_u32_u24 v92, v36, s5, v90
	ds_read2_b64 v[36:39], v91 offset0:48 offset1:64
	s_waitcnt lgkmcnt(1)
	v_pk_mul_f32 v[88:89], v[56:57], v[32:33] op_sel:[0,0] op_sel_hi:[0,1]
	v_pk_fma_f32 v[88:89], v[56:57], v[32:33], v[88:89] op_sel:[1,1,0] op_sel_hi:[1,0,1] neg_lo:[0,1,0]
	v_pk_mul_f32 v[56:57], v[44:45], v[34:35] op_sel:[0,0] op_sel_hi:[0,1]
	v_pk_fma_f32 v[56:57], v[44:45], v[34:35], v[56:57] op_sel:[1,1,0] op_sel_hi:[1,0,1] neg_lo:[0,1,0]
	s_waitcnt lgkmcnt(0)
	v_pk_mul_f32 v[44:45], v[46:47], v[36:37] op_sel:[0,0] op_sel_hi:[0,1]
	v_pk_fma_f32 v[44:45], v[46:47], v[36:37], v[44:45] op_sel:[1,1,0] op_sel_hi:[1,0,1] neg_lo:[0,1,0]
	ds_write2_b64 v92, v[56:57], v[44:45] offset0:32 offset1:48
	v_pk_mul_f32 v[44:45], v[66:67], v[38:39] op_sel:[0,0] op_sel_hi:[0,1]
	v_pk_fma_f32 v[44:45], v[66:67], v[38:39], v[44:45] op_sel:[1,1,0] op_sel_hi:[1,0,1] neg_lo:[0,1,0]
	ds_read2_b64 v[32:35], v91 offset0:80 offset1:96
	s_waitcnt lgkmcnt(0)
	v_pk_mul_f32 v[46:47], v[64:65], v[32:33] op_sel:[0,0] op_sel_hi:[0,1]
	v_pk_fma_f32 v[46:47], v[64:65], v[32:33], v[46:47] op_sel:[1,1,0] op_sel_hi:[1,0,1] neg_lo:[0,1,0]
	ds_write2_b64 v92, v[44:45], v[46:47] offset0:64 offset1:80
	v_pk_mul_f32 v[44:45], v[48:49], v[34:35] op_sel:[0,0] op_sel_hi:[0,1]
	v_pk_fma_f32 v[44:45], v[48:49], v[34:35], v[44:45] op_sel:[1,1,0] op_sel_hi:[1,0,1] neg_lo:[0,1,0]
	ds_read2_b64 v[36:39], v91 offset0:112 offset1:128
	ds_read2_b64 v[32:35], v91 offset0:144 offset1:160
	s_waitcnt lgkmcnt(1)
	v_pk_mul_f32 v[46:47], v[68:69], v[36:37] op_sel:[0,0] op_sel_hi:[0,1]
	v_pk_fma_f32 v[46:47], v[68:69], v[36:37], v[46:47] op_sel:[1,1,0] op_sel_hi:[1,0,1] neg_lo:[0,1,0]
	ds_write2_b64 v92, v[44:45], v[46:47] offset0:96 offset1:112
	v_pk_mul_f32 v[44:45], v[60:61], v[38:39] op_sel:[0,0] op_sel_hi:[0,1]
	v_pk_fma_f32 v[44:45], v[60:61], v[38:39], v[44:45] op_sel:[1,1,0] op_sel_hi:[1,0,1] neg_lo:[0,1,0]
	ds_read2_b64 v[36:39], v91 offset0:176 offset1:192
	s_waitcnt lgkmcnt(2)
	v_pk_mul_f32 v[46:47], v[54:55], v[32:33] op_sel:[0,0] op_sel_hi:[0,1]
	v_pk_fma_f32 v[46:47], v[54:55], v[32:33], v[46:47] op_sel:[1,1,0] op_sel_hi:[1,0,1] neg_lo:[0,1,0]
	ds_write2_b64 v92, v[44:45], v[46:47] offset0:128 offset1:144
	v_pk_mul_f32 v[44:45], v[42:43], v[34:35] op_sel:[0,0] op_sel_hi:[0,1]
	v_pk_fma_f32 v[44:45], v[42:43], v[34:35], v[44:45] op_sel:[1,1,0] op_sel_hi:[1,0,1] neg_lo:[0,1,0]
	ds_read2_b64 v[32:35], v91 offset0:208 offset1:224
	s_waitcnt lgkmcnt(2)
	v_pk_mul_f32 v[42:43], v[58:59], v[36:37] op_sel:[0,0] op_sel_hi:[0,1]
	v_pk_fma_f32 v[42:43], v[58:59], v[36:37], v[42:43] op_sel:[1,1,0] op_sel_hi:[1,0,1] neg_lo:[0,1,0]
	ds_write2_b64 v92, v[44:45], v[42:43] offset0:160 offset1:176
	v_pk_mul_f32 v[42:43], v[52:53], v[38:39] op_sel:[0,0] op_sel_hi:[0,1]
	v_pk_fma_f32 v[42:43], v[52:53], v[38:39], v[42:43] op_sel:[1,1,0] op_sel_hi:[1,0,1] neg_lo:[0,1,0]
	s_waitcnt lgkmcnt(1)
	v_pk_mul_f32 v[38:39], v[50:51], v[32:33] op_sel:[0,0] op_sel_hi:[0,1]
	v_pk_fma_f32 v[38:39], v[50:51], v[32:33], v[38:39] op_sel:[1,1,0] op_sel_hi:[1,0,1] neg_lo:[0,1,0]
	v_pk_mul_f32 v[32:33], v[40:41], v[34:35] op_sel:[0,0] op_sel_hi:[0,1]
	v_pk_fma_f32 v[32:33], v[40:41], v[34:35], v[32:33] op_sel:[1,1,0] op_sel_hi:[1,0,1] neg_lo:[0,1,0]
	ds_read_b64 v[36:37], v90 offset:36736
	s_waitcnt lgkmcnt(0)
	v_pk_mul_f32 v[34:35], v[86:87], v[36:37] op_sel:[0,0] op_sel_hi:[0,1]
	v_pk_fma_f32 v[34:35], v[86:87], v[36:37], v[34:35] op_sel:[1,1,0] op_sel_hi:[1,0,1] neg_lo:[0,1,0]
	ds_write2_b64 v92, v[32:33], v[34:35] offset0:224 offset1:240
	v_mov_b32_e32 v32, v0
	ds_write2_b64 v92, v[62:63], v[88:89] offset1:16
	ds_write2_b64 v92, v[42:43], v[38:39] offset0:192 offset1:208
	s_waitcnt lgkmcnt(0)
	s_barrier
	s_nop 0
	v_and_b32_e32 v33, 15, v32
	v_and_b32_e32 v32, 0x1ffffff0, v32
	v_lshlrev_b32_e32 v32, 3, v32
	v_mad_u32_u24 v60, v33, s5, v32
	ds_read2_b64 v[32:35], v60 offset1:1
	ds_read2_b64 v[36:39], v60 offset0:2 offset1:3
	ds_read2_b64 v[40:43], v60 offset0:8 offset1:9
	ds_read2_b64 v[44:47], v60 offset0:4 offset1:5
	ds_read2_b64 v[48:51], v60 offset0:6 offset1:7
	ds_read2_b64 v[52:55], v60 offset0:12 offset1:13
	ds_read2_b64 v[56:59], v60 offset0:10 offset1:11
	ds_read2_b64 v[60:63], v60 offset0:14 offset1:15
	s_waitcnt lgkmcnt(5)
	v_pk_add_f32 v[64:65], v[32:33], v[40:41]
	v_pk_add_f32 v[32:33], v[32:33], v[40:41] neg_lo:[0,1] neg_hi:[0,1]
	s_waitcnt lgkmcnt(2)
	v_pk_add_f32 v[40:41], v[44:45], v[52:53]
	v_pk_add_f32 v[44:45], v[44:45], v[52:53] neg_lo:[0,1] neg_hi:[0,1]
	v_pk_add_f32 v[52:53], v[64:65], v[40:41]
	v_pk_add_f32 v[40:41], v[64:65], v[40:41] neg_lo:[0,1] neg_hi:[0,1]
	v_pk_add_f32 v[64:65], v[32:33], v[44:45] op_sel:[0,1] op_sel_hi:[1,0] neg_hi:[0,1]
	v_pk_add_f32 v[66:67], v[32:33], v[44:45] op_sel:[0,1] op_sel_hi:[1,0] neg_lo:[0,1]
	v_pk_add_f32 v[32:33], v[34:35], v[42:43]
	v_pk_add_f32 v[34:35], v[34:35], v[42:43] neg_lo:[0,1] neg_hi:[0,1]
	v_pk_add_f32 v[42:43], v[46:47], v[54:55]
	v_pk_add_f32 v[44:45], v[46:47], v[54:55] neg_lo:[0,1] neg_hi:[0,1]
	v_pk_add_f32 v[46:47], v[32:33], v[42:43]
	v_pk_add_f32 v[32:33], v[32:33], v[42:43] neg_lo:[0,1] neg_hi:[0,1]
	v_pk_add_f32 v[42:43], v[34:35], v[44:45] op_sel:[0,1] op_sel_hi:[1,0] neg_hi:[0,1]
	v_pk_add_f32 v[34:35], v[34:35], v[44:45] op_sel:[0,1] op_sel_hi:[1,0] neg_lo:[0,1]
	s_waitcnt lgkmcnt(1)
	v_pk_add_f32 v[44:45], v[36:37], v[56:57]
	s_waitcnt lgkmcnt(0)
	v_pk_add_f32 v[54:55], v[48:49], v[60:61]
	v_pk_add_f32 v[32:33], v[32:33], v[32:33] op_sel:[0,1] op_sel_hi:[1,0] neg_hi:[0,1]
	v_pk_add_f32 v[36:37], v[36:37], v[56:57] neg_lo:[0,1] neg_hi:[0,1]
	v_pk_add_f32 v[48:49], v[48:49], v[60:61] neg_lo:[0,1] neg_hi:[0,1]
	v_pk_add_f32 v[56:57], v[44:45], v[54:55]
	v_pk_add_f32 v[54:55], v[44:45], v[54:55] neg_lo:[0,1] neg_hi:[0,1]
	v_pk_add_f32 v[44:45], v[36:37], v[48:49] op_sel:[0,1] op_sel_hi:[1,0] neg_hi:[0,1]
	v_pk_mul_f32 v[68:69], v[32:33], s[8:9]
	v_pk_add_f32 v[36:37], v[36:37], v[48:49] op_sel:[0,1] op_sel_hi:[1,0] neg_lo:[0,1]
	v_pk_add_f32 v[48:49], v[38:39], v[58:59]
	v_pk_add_f32 v[32:33], v[44:45], v[44:45] op_sel:[0,1] op_sel_hi:[1,0] neg_hi:[0,1]
	v_pk_add_f32 v[38:39], v[38:39], v[58:59] neg_lo:[0,1] neg_hi:[0,1]
	v_pk_add_f32 v[58:59], v[50:51], v[62:63]
	v_pk_mul_f32 v[86:87], v[34:35], s[10:11] op_sel:[0,0] op_sel_hi:[0,1]
	v_pk_fma_f32 v[86:87], v[34:35], s[10:11], v[86:87] op_sel:[1,1,0] op_sel_hi:[1,0,1] neg_lo:[0,1,0]
	v_pk_mul_f32 v[34:35], v[32:33], s[8:9]
	v_pk_add_f32 v[32:33], v[36:37], v[36:37] op_sel:[0,1] op_sel_hi:[1,0] neg_lo:[0,1]
	v_pk_add_f32 v[50:51], v[50:51], v[62:63] neg_lo:[0,1] neg_hi:[0,1]
	v_pk_add_f32 v[60:61], v[48:49], v[58:59]
	v_pk_add_f32 v[48:49], v[48:49], v[58:59] neg_lo:[0,1] neg_hi:[0,1]
	v_pk_add_f32 v[58:59], v[38:39], v[50:51] op_sel:[0,1] op_sel_hi:[1,0] neg_hi:[0,1]
	v_pk_add_f32 v[38:39], v[38:39], v[50:51] op_sel:[0,1] op_sel_hi:[1,0] neg_lo:[0,1]
	v_pk_mul_f32 v[88:89], v[32:33], s[12:13]
	v_pk_add_f32 v[36:37], v[46:47], v[60:61]
	v_pk_add_f32 v[32:33], v[48:49], v[48:49] op_sel:[0,1] op_sel_hi:[1,0] neg_lo:[0,1]
	v_pk_mul_f32 v[44:45], v[58:59], s[10:11] op_sel:[0,0] op_sel_hi:[0,1]
	v_pk_fma_f32 v[44:45], v[58:59], s[10:11], v[44:45] op_sel:[1,1,0] op_sel_hi:[1,0,1] neg_lo:[0,1,0]
	v_pk_mul_f32 v[58:59], v[38:39], s[14:15] op_sel:[0,0] op_sel_hi:[0,1]
	v_pk_fma_f32 v[58:59], v[38:39], s[14:15], v[58:59] op_sel:[1,1,0] op_sel_hi:[1,0,1] neg_lo:[0,1,0]
	v_pk_add_f32 v[38:39], v[52:53], v[56:57] neg_lo:[0,1] neg_hi:[0,1]
	v_pk_mul_f32 v[48:49], v[32:33], s[12:13]
	v_pk_add_f32 v[32:33], v[52:53], v[56:57]
	v_pk_add_f32 v[46:47], v[46:47], v[60:61] neg_lo:[0,1] neg_hi:[0,1]
	v_pk_mul_f32 v[62:63], v[42:43], s[6:7] op_sel:[0,0] op_sel_hi:[0,1]
	v_pk_fma_f32 v[62:63], v[42:43], s[6:7], v[62:63] op_sel:[1,1,0] op_sel_hi:[1,0,1] neg_lo:[0,1,0]
	v_pk_add_f32 v[50:51], v[32:33], v[36:37]
	v_pk_add_f32 v[36:37], v[32:33], v[36:37] neg_lo:[0,1] neg_hi:[0,1]
	v_pk_add_f32 v[42:43], v[38:39], v[46:47] op_sel:[0,1] op_sel_hi:[1,0] neg_hi:[0,1]
	v_pk_add_f32 v[32:33], v[38:39], v[46:47] op_sel:[0,1] op_sel_hi:[1,0] neg_lo:[0,1]
	v_pk_add_f32 v[38:39], v[64:65], v[34:35]
	v_pk_add_f32 v[34:35], v[64:65], v[34:35] neg_lo:[0,1] neg_hi:[0,1]
	v_pk_add_f32 v[46:47], v[62:63], v[44:45]
	v_pk_add_f32 v[56:57], v[62:63], v[44:45] neg_lo:[0,1] neg_hi:[0,1]
	v_pk_add_f32 v[52:53], v[38:39], v[46:47]
	v_pk_add_f32 v[38:39], v[38:39], v[46:47] neg_lo:[0,1] neg_hi:[0,1]
	v_pk_add_f32 v[44:45], v[34:35], v[56:57] op_sel:[0,1] op_sel_hi:[1,0] neg_hi:[0,1]
	v_pk_add_f32 v[34:35], v[34:35], v[56:57] op_sel:[0,1] op_sel_hi:[1,0] neg_lo:[0,1]
	v_pk_add_f32 v[46:47], v[40:41], v[54:55] op_sel:[0,1] op_sel_hi:[1,0] neg_hi:[0,1]
	v_pk_add_f32 v[56:57], v[40:41], v[54:55] op_sel:[0,1] op_sel_hi:[1,0] neg_lo:[0,1]
	v_pk_add_f32 v[40:41], v[68:69], v[48:49]
	v_pk_add_f32 v[60:61], v[68:69], v[48:49] neg_lo:[0,1] neg_hi:[0,1]
	v_pk_add_f32 v[54:55], v[40:41], v[46:47]
	v_pk_add_f32 v[40:41], v[46:47], v[40:41] neg_lo:[0,1] neg_hi:[0,1]
	v_pk_add_f32 v[46:47], v[66:67], v[88:89]
	v_pk_add_f32 v[62:63], v[86:87], v[58:59]
	v_pk_add_f32 v[58:59], v[86:87], v[58:59] neg_lo:[0,1] neg_hi:[0,1]
	v_pk_add_f32 v[48:49], v[56:57], v[60:61] op_sel:[0,1] op_sel_hi:[1,0] neg_hi:[0,1]
	v_pk_add_f32 v[64:65], v[56:57], v[60:61] op_sel:[0,1] op_sel_hi:[1,0] neg_lo:[0,1]
	v_pk_add_f32 v[60:61], v[66:67], v[88:89] neg_lo:[0,1] neg_hi:[0,1]
	v_pk_add_f32 v[56:57], v[46:47], v[62:63]
	v_pk_add_f32 v[68:69], v[46:47], v[62:63] neg_lo:[0,1] neg_hi:[0,1]
	v_pk_add_f32 v[46:47], v[60:61], v[58:59] op_sel:[0,1] op_sel_hi:[1,0] neg_hi:[0,1]
	v_pk_add_f32 v[66:67], v[60:61], v[58:59] op_sel:[0,1] op_sel_hi:[1,0] neg_lo:[0,1]
	v_mov_b32_e32 v58, v0
	s_nop 0
	v_and_b32_e32 v59, -16, v58
	v_and_b32_e32 v60, 15, v58
	v_lshlrev_b32_e32 v61, 3, v59
	v_mad_u32_u24 v61, v60, s5, v61
	v_cmp_ne_u32_e32 vcc, 0, v60
	ds_write2_b64 v61, v[50:51], v[52:53] offset1:1
	ds_write2_b64 v61, v[54:55], v[56:57] offset0:2 offset1:3
	ds_write2_b64 v61, v[42:43], v[44:45] offset0:4 offset1:5
	ds_write2_b64 v61, v[48:49], v[46:47] offset0:6 offset1:7
	ds_write2_b64 v61, v[36:37], v[38:39] offset0:8 offset1:9
	ds_write2_b64 v61, v[40:41], v[68:69] offset0:10 offset1:11
	ds_write2_b64 v61, v[32:33], v[34:35] offset0:12 offset1:13
	ds_write2_b64 v61, v[64:65], v[66:67] offset0:14 offset1:15
	s_waitcnt lgkmcnt(0)
	s_barrier
	s_and_saveexec_b64 s[6:7], vcc
	s_xor_b64 s[6:7], exec, s[6:7]
	v_sub_u32_e32 v60, 16, v60
	v_mul_u32_u24_e32 v60, 0x111, v60
	v_sub_u32_e32 v59, v60, v59
	v_add_u32_e32 v61, 0xf0, v59
	s_andn2_saveexec_b64 s[6:7], s[6:7]
	v_sub_u32_e32 v59, 0x100, v58
	v_cmp_lt_u32_e32 vcc, 15, v58
	s_nop 1
	v_cndmask_b32_e32 v61, 1, v59, vcc
	s_or_b64 exec, exec, s[6:7]
	v_mov_b32_e32 v59, 0
	v_lshlrev_b32_e32 v92, 3, v61
	ds_read_b64 v[90:91], v59
	ds_read2_b64 v[60:63], v92 offset0:14 offset1:15
	ds_read2_b64 v[86:89], v92 offset0:12 offset1:13
	v_cmp_eq_u32_e32 vcc, 0, v58
	v_cvt_f32_fp8_sdwa v93, v74 src0_sel:BYTE_3
	v_cvt_f32_fp8_sdwa v94, v72 src0_sel:BYTE_1
	s_waitcnt lgkmcnt(1)
	v_cndmask_b32_e32 v59, v63, v91, vcc
	v_cndmask_b32_e32 v58, v62, v90, vcc
	v_pk_add_f32 v[90:91], v[50:51], v[58:59] neg_hi:[0,1]
	v_pk_add_f32 v[50:51], v[50:51], v[58:59] neg_lo:[0,1]
	v_cvt_f32_fp8_sdwa v95, v72 src0_sel:BYTE_3
	v_pk_mul_f32 v[62:63], v[90:91], v[50:51] op_sel:[0,0] op_sel_hi:[0,1]
	v_pk_fma_f32 v[62:63], v[90:91], v[50:51], v[62:63] op_sel:[1,1,0] op_sel_hi:[1,0,1] neg_hi:[0,1,0]
	v_pk_add_f32 v[50:51], v[52:53], v[60:61] neg_hi:[0,1]
	v_pk_add_f32 v[52:53], v[52:53], v[60:61] neg_lo:[0,1]
	v_cvt_f32_fp8_sdwa v72, v71 src0_sel:BYTE_1
	v_pk_mul_f32 v[60:61], v[50:51], v[52:53] op_sel:[0,0] op_sel_hi:[0,1]
	v_pk_fma_f32 v[60:61], v[50:51], v[52:53], v[60:61] op_sel:[1,1,0] op_sel_hi:[1,0,1] neg_hi:[0,1,0]
	s_waitcnt lgkmcnt(0)
	v_pk_add_f32 v[50:51], v[54:55], v[88:89] neg_hi:[0,1]
	v_pk_add_f32 v[52:53], v[54:55], v[88:89] neg_lo:[0,1]
	v_pk_add_f32 v[54:55], v[56:57], v[86:87] neg_hi:[0,1]
	v_pk_add_f32 v[86:87], v[56:57], v[86:87] neg_lo:[0,1]
	v_cvt_f32_fp8_sdwa v98, v70 src0_sel:BYTE_1
	v_pk_mul_f32 v[58:59], v[50:51], v[52:53] op_sel:[0,0] op_sel_hi:[0,1]
	v_pk_fma_f32 v[58:59], v[50:51], v[52:53], v[58:59] op_sel:[1,1,0] op_sel_hi:[1,0,1] neg_hi:[0,1,0]
	ds_read2_b64 v[50:53], v92 offset0:10 offset1:11
	v_pk_mul_f32 v[56:57], v[54:55], v[86:87] op_sel:[0,0] op_sel_hi:[0,1]
	v_pk_fma_f32 v[56:57], v[54:55], v[86:87], v[56:57] op_sel:[1,1,0] op_sel_hi:[1,0,1] neg_hi:[0,1,0]
	ds_read2_b64 v[86:89], v92 offset0:8 offset1:9
	s_waitcnt lgkmcnt(1)
	v_pk_add_f32 v[90:91], v[42:43], v[52:53] neg_hi:[0,1]
	v_pk_add_f32 v[42:43], v[42:43], v[52:53] neg_lo:[0,1]
	v_cvt_f32_fp8_sdwa v99, v70 src0_sel:BYTE_3
	v_pk_mul_f32 v[54:55], v[90:91], v[42:43] op_sel:[0,0] op_sel_hi:[0,1]
	v_pk_fma_f32 v[54:55], v[90:91], v[42:43], v[54:55] op_sel:[1,1,0] op_sel_hi:[1,0,1] neg_hi:[0,1,0]
	v_pk_add_f32 v[42:43], v[44:45], v[50:51] neg_hi:[0,1]
	v_pk_add_f32 v[44:45], v[44:45], v[50:51] neg_lo:[0,1]
	s_mov_b32 s6, 0x3f6c835e
	v_pk_mul_f32 v[52:53], v[42:43], v[44:45] op_sel:[0,0] op_sel_hi:[0,1]
	v_pk_fma_f32 v[52:53], v[42:43], v[44:45], v[52:53] op_sel:[1,1,0] op_sel_hi:[1,0,1] neg_hi:[0,1,0]
	s_waitcnt lgkmcnt(0)
	v_pk_add_f32 v[42:43], v[48:49], v[88:89] neg_hi:[0,1]
	v_pk_add_f32 v[44:45], v[48:49], v[88:89] neg_lo:[0,1]
	v_pk_add_f32 v[88:89], v[46:47], v[86:87] neg_hi:[0,1]
	v_pk_add_f32 v[46:47], v[46:47], v[86:87] neg_lo:[0,1]
	s_mov_b32 s7, 0xbec3ef15
	v_pk_mul_f32 v[50:51], v[42:43], v[44:45] op_sel:[0,0] op_sel_hi:[0,1]
	v_pk_fma_f32 v[50:51], v[42:43], v[44:45], v[50:51] op_sel:[1,1,0] op_sel_hi:[1,0,1] neg_hi:[0,1,0]
	ds_read2_b64 v[42:45], v92 offset0:6 offset1:7
	v_pk_mul_f32 v[48:49], v[88:89], v[46:47] op_sel:[0,0] op_sel_hi:[0,1]
	v_pk_fma_f32 v[48:49], v[88:89], v[46:47], v[48:49] op_sel:[1,1,0] op_sel_hi:[1,0,1] neg_hi:[0,1,0]
	ds_read2_b64 v[86:89], v92 offset0:4 offset1:5
	s_waitcnt lgkmcnt(1)
	v_pk_add_f32 v[90:91], v[36:37], v[44:45] neg_hi:[0,1]
	v_pk_add_f32 v[36:37], v[36:37], v[44:45] neg_lo:[0,1]
	s_mov_b32 s9, s8
	v_pk_mul_f32 v[46:47], v[90:91], v[36:37] op_sel:[0,0] op_sel_hi:[0,1]
	v_pk_fma_f32 v[46:47], v[90:91], v[36:37], v[46:47] op_sel:[1,1,0] op_sel_hi:[1,0,1] neg_hi:[0,1,0]
	v_pk_add_f32 v[36:37], v[38:39], v[42:43] neg_hi:[0,1]
	v_pk_add_f32 v[38:39], v[38:39], v[42:43] neg_lo:[0,1]
	v_cvt_f32_fp8_sdwa v90, v76 src0_sel:BYTE_1
	v_pk_mul_f32 v[44:45], v[36:37], v[38:39] op_sel:[0,0] op_sel_hi:[0,1]
	v_pk_fma_f32 v[44:45], v[36:37], v[38:39], v[44:45] op_sel:[1,1,0] op_sel_hi:[1,0,1] neg_hi:[0,1,0]
	s_waitcnt lgkmcnt(0)
	v_pk_add_f32 v[36:37], v[40:41], v[88:89] neg_hi:[0,1]
	v_pk_add_f32 v[38:39], v[40:41], v[88:89] neg_lo:[0,1]
	v_pk_add_f32 v[88:89], v[68:69], v[86:87] neg_hi:[0,1]
	v_pk_add_f32 v[68:69], v[68:69], v[86:87] neg_lo:[0,1]
	v_cvt_f32_fp8_sdwa v91, v76 src0_sel:BYTE_3
	v_pk_mul_f32 v[42:43], v[36:37], v[38:39] op_sel:[0,0] op_sel_hi:[0,1]
	v_pk_fma_f32 v[42:43], v[36:37], v[38:39], v[42:43] op_sel:[1,1,0] op_sel_hi:[1,0,1] neg_hi:[0,1,0]
	ds_read2_b64 v[36:39], v92 offset0:2 offset1:3
	v_pk_mul_f32 v[40:41], v[88:89], v[68:69] op_sel:[0,0] op_sel_hi:[0,1]
	v_pk_fma_f32 v[40:41], v[88:89], v[68:69], v[40:41] op_sel:[1,1,0] op_sel_hi:[1,0,1] neg_hi:[0,1,0]
	ds_read2_b64 v[86:89], v92 offset1:1
	s_waitcnt lgkmcnt(1)
	v_pk_add_f32 v[68:69], v[32:33], v[38:39] neg_hi:[0,1]
	v_pk_add_f32 v[32:33], v[32:33], v[38:39] neg_lo:[0,1]
	v_cvt_f32_fp8_sdwa v76, v75 src0_sel:BYTE_1
	v_pk_mul_f32 v[38:39], v[68:69], v[32:33] op_sel:[0,0] op_sel_hi:[0,1]
	v_pk_fma_f32 v[38:39], v[68:69], v[32:33], v[38:39] op_sel:[1,1,0] op_sel_hi:[1,0,1] neg_hi:[0,1,0]
	v_pk_add_f32 v[32:33], v[34:35], v[36:37] neg_hi:[0,1]
	v_pk_add_f32 v[34:35], v[34:35], v[36:37] neg_lo:[0,1]
	v_cvt_f32_fp8_sdwa v68, v83 src0_sel:BYTE_1
	v_pk_mul_f32 v[36:37], v[32:33], v[34:35] op_sel:[0,0] op_sel_hi:[0,1]
	v_pk_fma_f32 v[36:37], v[32:33], v[34:35], v[36:37] op_sel:[1,1,0] op_sel_hi:[1,0,1] neg_hi:[0,1,0]
	s_waitcnt lgkmcnt(0)
	v_pk_add_f32 v[32:33], v[64:65], v[88:89] neg_hi:[0,1]
	v_pk_add_f32 v[64:65], v[64:65], v[88:89] neg_lo:[0,1]
	v_cvt_f32_fp8_sdwa v69, v83 src0_sel:BYTE_3
	v_pk_mul_f32 v[34:35], v[32:33], v[64:65] op_sel:[0,0] op_sel_hi:[0,1]
	v_pk_fma_f32 v[34:35], v[32:33], v[64:65], v[34:35] op_sel:[1,1,0] op_sel_hi:[1,0,1] neg_hi:[0,1,0]
	v_pk_add_f32 v[64:65], v[66:67], v[86:87] neg_hi:[0,1]
	v_pk_add_f32 v[66:67], v[66:67], v[86:87] neg_lo:[0,1]
	v_cvt_f32_fp8_sdwa v83, v81 src0_sel:BYTE_3
	v_pk_mul_f32 v[32:33], v[64:65], v[66:67] op_sel:[0,0] op_sel_hi:[0,1]
	v_pk_fma_f32 v[32:33], v[64:65], v[66:67], v[32:33] op_sel:[1,1,0] op_sel_hi:[1,0,1] neg_hi:[0,1,0]
	v_cvt_f32_fp8_sdwa v64, v85 src0_sel:BYTE_1
	v_cvt_f32_fp8_sdwa v65, v85 src0_sel:BYTE_3
	v_cvt_f32_fp8_sdwa v66, v84 src0_sel:BYTE_1
	v_cvt_f32_fp8_sdwa v67, v84 src0_sel:BYTE_3
	v_cvt_f32_fp8_sdwa v84, v82 src0_sel:BYTE_1
	v_cvt_f32_fp8_sdwa v85, v82 src0_sel:BYTE_3
	v_cvt_f32_fp8_sdwa v82, v81 src0_sel:BYTE_1
	v_cvt_f32_fp8_sdwa v86, v80 src0_sel:BYTE_1
	v_cvt_f32_fp8_sdwa v87, v80 src0_sel:BYTE_3
	v_cvt_f32_fp8_sdwa v80, v79 src0_sel:BYTE_1
	v_cvt_f32_fp8_sdwa v81, v79 src0_sel:BYTE_3
	v_cvt_f32_fp8_sdwa v88, v78 src0_sel:BYTE_1
	v_cvt_f32_fp8_sdwa v89, v78 src0_sel:BYTE_3
	v_cvt_f32_fp8_sdwa v78, v77 src0_sel:BYTE_1
	v_cvt_f32_fp8_sdwa v79, v77 src0_sel:BYTE_3
	v_cvt_f32_fp8_sdwa v77, v75 src0_sel:BYTE_3
	v_cvt_f32_fp8_sdwa v92, v74 src0_sel:BYTE_1
	v_cvt_f32_fp8_sdwa v74, v73 src0_sel:BYTE_1
	v_cvt_f32_fp8_sdwa v75, v73 src0_sel:BYTE_3
	v_cvt_f32_fp8_sdwa v73, v71 src0_sel:BYTE_3
	v_pk_add_f32 v[70:71], v[64:65], v[78:79]
	v_pk_add_f32 v[64:65], v[64:65], v[78:79] neg_lo:[0,1] neg_hi:[0,1]
	v_pk_add_f32 v[78:79], v[82:83], v[74:75]
	v_pk_add_f32 v[74:75], v[82:83], v[74:75] neg_lo:[0,1] neg_hi:[0,1]
	v_pk_add_f32 v[82:83], v[70:71], v[78:79]
	v_pk_add_f32 v[70:71], v[70:71], v[78:79] neg_lo:[0,1] neg_hi:[0,1]
	v_pk_add_f32 v[78:79], v[64:65], v[74:75] op_sel:[0,1] op_sel_hi:[1,0] neg_hi:[0,1]
	v_pk_add_f32 v[64:65], v[64:65], v[74:75] op_sel:[0,1] op_sel_hi:[1,0] neg_lo:[0,1]
	v_pk_add_f32 v[74:75], v[66:67], v[90:91]
	v_pk_add_f32 v[66:67], v[66:67], v[90:91] neg_lo:[0,1] neg_hi:[0,1]
	v_pk_add_f32 v[90:91], v[86:87], v[94:95]
	v_pk_add_f32 v[86:87], v[86:87], v[94:95] neg_lo:[0,1] neg_hi:[0,1]
	v_pk_add_f32 v[94:95], v[74:75], v[90:91]
	v_pk_add_f32 v[74:75], v[74:75], v[90:91] neg_lo:[0,1] neg_hi:[0,1]
	v_pk_add_f32 v[90:91], v[66:67], v[86:87] op_sel:[0,1] op_sel_hi:[1,0] neg_hi:[0,1]
	v_pk_add_f32 v[66:67], v[66:67], v[86:87] op_sel:[0,1] op_sel_hi:[1,0] neg_lo:[0,1]
	v_pk_add_f32 v[86:87], v[68:69], v[76:77]
	v_pk_add_f32 v[68:69], v[68:69], v[76:77] neg_lo:[0,1] neg_hi:[0,1]
	v_pk_add_f32 v[76:77], v[80:81], v[72:73]
	v_pk_add_f32 v[72:73], v[80:81], v[72:73] neg_lo:[0,1] neg_hi:[0,1]
	v_pk_add_f32 v[80:81], v[86:87], v[76:77]
	v_pk_add_f32 v[76:77], v[86:87], v[76:77] neg_lo:[0,1] neg_hi:[0,1]
	v_pk_add_f32 v[86:87], v[68:69], v[72:73] op_sel:[0,1] op_sel_hi:[1,0] neg_hi:[0,1]
	v_pk_add_f32 v[68:69], v[68:69], v[72:73] op_sel:[0,1] op_sel_hi:[1,0] neg_lo:[0,1]
	v_pk_add_f32 v[72:73], v[84:85], v[92:93]
	v_pk_add_f32 v[84:85], v[84:85], v[92:93] neg_lo:[0,1] neg_hi:[0,1]
	v_pk_add_f32 v[92:93], v[88:89], v[98:99]
	v_pk_add_f32 v[88:89], v[88:89], v[98:99] neg_lo:[0,1] neg_hi:[0,1]
	v_pk_add_f32 v[98:99], v[72:73], v[92:93]
	v_pk_add_f32 v[72:73], v[72:73], v[92:93] neg_lo:[0,1] neg_hi:[0,1]
	v_pk_add_f32 v[92:93], v[84:85], v[88:89] op_sel:[0,1] op_sel_hi:[1,0] neg_hi:[0,1]
	v_pk_add_f32 v[84:85], v[84:85], v[88:89] op_sel:[0,1] op_sel_hi:[1,0] neg_lo:[0,1]
	v_pk_mul_f32 v[88:89], v[90:91], s[6:7] op_sel:[0,0] op_sel_hi:[0,1]
	v_pk_fma_f32 v[88:89], v[90:91], s[6:7], v[88:89] op_sel:[1,1,0] op_sel_hi:[1,0,1] neg_lo:[0,1,0]
	v_pk_mul_f32 v[90:91], v[66:67], s[10:11] op_sel:[0,0] op_sel_hi:[0,1]
	v_pk_fma_f32 v[90:91], v[66:67], s[10:11], v[90:91] op_sel:[1,1,0] op_sel_hi:[1,0,1] neg_lo:[0,1,0]
	v_pk_add_f32 v[66:67], v[86:87], v[86:87] op_sel:[0,1] op_sel_hi:[1,0] neg_hi:[0,1]
	s_nop 0
	v_pk_add_f32 v[72:73], v[72:73], v[72:73] op_sel:[0,1] op_sel_hi:[1,0] neg_lo:[0,1]
	v_pk_mul_f32 v[86:87], v[92:93], s[10:11] op_sel:[0,0] op_sel_hi:[0,1]
	v_pk_fma_f32 v[86:87], v[92:93], s[10:11], v[86:87] op_sel:[1,1,0] op_sel_hi:[1,0,1] neg_lo:[0,1,0]
	s_mov_b32 s14, s11
	v_pk_mul_f32 v[66:67], v[66:67], s[8:9]
	s_mov_b32 s15, s10
	v_pk_mul_f32 v[92:93], v[84:85], s[14:15] op_sel:[0,0] op_sel_hi:[0,1]
	v_pk_fma_f32 v[92:93], v[84:85], s[14:15], v[92:93] op_sel:[1,1,0] op_sel_hi:[1,0,1] neg_lo:[0,1,0]
	v_pk_add_f32 v[84:85], v[82:83], v[80:81]
	v_pk_add_f32 v[80:81], v[82:83], v[80:81] neg_lo:[0,1] neg_hi:[0,1]
	v_pk_add_f32 v[82:83], v[94:95], v[98:99]
	v_pk_add_f32 v[94:95], v[94:95], v[98:99] neg_lo:[0,1] neg_hi:[0,1]
	v_pk_add_f32 v[74:75], v[74:75], v[74:75] op_sel:[0,1] op_sel_hi:[1,0] neg_hi:[0,1]
	v_pk_add_f32 v[68:69], v[68:69], v[68:69] op_sel:[0,1] op_sel_hi:[1,0] neg_lo:[0,1]
	s_mov_b32 s13, s12
	v_pk_mul_f32 v[72:73], v[72:73], s[12:13]
	v_pk_add_f32 v[98:99], v[84:85], v[82:83]
	v_pk_add_f32 v[82:83], v[84:85], v[82:83] neg_lo:[0,1] neg_hi:[0,1]
	v_pk_add_f32 v[84:85], v[80:81], v[94:95] op_sel:[0,1] op_sel_hi:[1,0] neg_hi:[0,1]
	v_pk_add_f32 v[80:81], v[80:81], v[94:95] op_sel:[0,1] op_sel_hi:[1,0] neg_lo:[0,1]
	v_pk_add_f32 v[94:95], v[78:79], v[66:67]
	v_pk_add_f32 v[66:67], v[78:79], v[66:67] neg_lo:[0,1] neg_hi:[0,1]
	v_pk_add_f32 v[78:79], v[88:89], v[86:87]
	v_pk_add_f32 v[86:87], v[88:89], v[86:87] neg_lo:[0,1] neg_hi:[0,1]
	v_pk_mul_f32 v[74:75], v[74:75], s[8:9]
	v_pk_mul_f32 v[68:69], v[68:69], s[12:13]
	v_pk_add_f32 v[88:89], v[94:95], v[78:79]
	v_pk_add_f32 v[78:79], v[94:95], v[78:79] neg_lo:[0,1] neg_hi:[0,1]
	v_pk_add_f32 v[94:95], v[66:67], v[86:87] op_sel:[0,1] op_sel_hi:[1,0] neg_hi:[0,1]
	v_pk_add_f32 v[66:67], v[66:67], v[86:87] op_sel:[0,1] op_sel_hi:[1,0] neg_lo:[0,1]
	v_pk_add_f32 v[86:87], v[70:71], v[76:77] op_sel:[0,1] op_sel_hi:[1,0] neg_hi:[0,1]
	v_pk_add_f32 v[70:71], v[70:71], v[76:77] op_sel:[0,1] op_sel_hi:[1,0] neg_lo:[0,1]
	v_pk_add_f32 v[76:77], v[74:75], v[72:73]
	v_pk_add_f32 v[72:73], v[74:75], v[72:73] neg_lo:[0,1] neg_hi:[0,1]
	v_pk_add_f32 v[74:75], v[76:77], v[86:87]
	v_pk_add_f32 v[76:77], v[86:87], v[76:77] neg_lo:[0,1] neg_hi:[0,1]
	v_pk_add_f32 v[86:87], v[70:71], v[72:73] op_sel:[0,1] op_sel_hi:[1,0] neg_hi:[0,1]
	v_pk_add_f32 v[70:71], v[70:71], v[72:73] op_sel:[0,1] op_sel_hi:[1,0] neg_lo:[0,1]
	v_pk_add_f32 v[72:73], v[64:65], v[68:69]
	v_pk_add_f32 v[64:65], v[64:65], v[68:69] neg_lo:[0,1] neg_hi:[0,1]
	v_pk_add_f32 v[68:69], v[90:91], v[92:93]
	v_pk_add_f32 v[90:91], v[90:91], v[92:93] neg_lo:[0,1] neg_hi:[0,1]
	v_pk_add_f32 v[92:93], v[72:73], v[68:69]
	v_pk_add_f32 v[68:69], v[72:73], v[68:69] neg_lo:[0,1] neg_hi:[0,1]
	v_pk_add_f32 v[72:73], v[64:65], v[90:91] op_sel:[0,1] op_sel_hi:[1,0] neg_hi:[0,1]
	v_pk_add_f32 v[64:65], v[64:65], v[90:91] op_sel:[0,1] op_sel_hi:[1,0] neg_lo:[0,1]
	v_pk_mul_f32 v[90:91], v[88:89], v[30:31] op_sel:[0,0] op_sel_hi:[0,1]
	v_pk_fma_f32 v[90:91], v[88:89], v[30:31], v[90:91] op_sel:[1,1,0] op_sel_hi:[1,0,1] neg_lo:[0,1,0]
	v_pk_mul_f32 v[88:89], v[74:75], v[28:29] op_sel:[0,0] op_sel_hi:[0,1]
	v_pk_fma_f32 v[88:89], v[74:75], v[28:29], v[88:89] op_sel:[1,1,0] op_sel_hi:[1,0,1] neg_lo:[0,1,0]
	v_pk_mul_f32 v[74:75], v[92:93], v[26:27] op_sel:[0,0] op_sel_hi:[0,1]
	v_pk_fma_f32 v[74:75], v[92:93], v[26:27], v[74:75] op_sel:[1,1,0] op_sel_hi:[1,0,1] neg_lo:[0,1,0]
	s_barrier
	ds_write_b64 v1, v[74:75] offset:6552
	v_pk_mul_f32 v[74:75], v[84:85], v[24:25] op_sel:[0,0] op_sel_hi:[0,1]
	v_pk_fma_f32 v[74:75], v[84:85], v[24:25], v[74:75] op_sel:[1,1,0] op_sel_hi:[1,0,1] neg_lo:[0,1,0]
	ds_write_b64 v1, v[74:75] offset:8736
	v_pk_mul_f32 v[74:75], v[94:95], v[20:21] op_sel:[0,0] op_sel_hi:[0,1]
	v_pk_fma_f32 v[74:75], v[94:95], v[20:21], v[74:75] op_sel:[1,1,0] op_sel_hi:[1,0,1] neg_lo:[0,1,0]
	ds_write_b64 v1, v[74:75] offset:10920
	v_pk_mul_f32 v[74:75], v[86:87], v[16:17] op_sel:[0,0] op_sel_hi:[0,1]
	v_pk_fma_f32 v[74:75], v[86:87], v[16:17], v[74:75] op_sel:[1,1,0] op_sel_hi:[1,0,1] neg_lo:[0,1,0]
	ds_write_b64 v1, v[74:75] offset:13104
	v_pk_mul_f32 v[74:75], v[72:73], v[10:11] op_sel:[0,0] op_sel_hi:[0,1]
	v_pk_fma_f32 v[74:75], v[72:73], v[10:11], v[74:75] op_sel:[1,1,0] op_sel_hi:[1,0,1] neg_lo:[0,1,0]
	v_pk_mul_f32 v[72:73], v[82:83], v[22:23] op_sel:[0,0] op_sel_hi:[0,1]
	v_pk_fma_f32 v[72:73], v[82:83], v[22:23], v[72:73] op_sel:[1,1,0] op_sel_hi:[1,0,1] neg_lo:[0,1,0]
	ds_write_b64 v1, v[72:73] offset:17472
	v_pk_mul_f32 v[72:73], v[78:79], v[18:19] op_sel:[0,0] op_sel_hi:[0,1]
	v_pk_fma_f32 v[72:73], v[78:79], v[18:19], v[72:73] op_sel:[1,1,0] op_sel_hi:[1,0,1] neg_lo:[0,1,0]
	ds_write_b64 v1, v[72:73] offset:19656
	v_pk_mul_f32 v[72:73], v[76:77], v[12:13] op_sel:[0,0] op_sel_hi:[0,1]
	v_pk_fma_f32 v[72:73], v[76:77], v[12:13], v[72:73] op_sel:[1,1,0] op_sel_hi:[1,0,1] neg_lo:[0,1,0]
	ds_write_b64 v1, v[72:73] offset:21840
	v_pk_mul_f32 v[72:73], v[68:69], v[14:15] op_sel:[0,0] op_sel_hi:[0,1]
	v_pk_fma_f32 v[72:73], v[68:69], v[14:15], v[72:73] op_sel:[1,1,0] op_sel_hi:[1,0,1] neg_lo:[0,1,0]
	v_pk_mul_f32 v[68:69], v[80:81], v[6:7] op_sel:[0,0] op_sel_hi:[0,1]
	v_pk_fma_f32 v[68:69], v[80:81], v[6:7], v[68:69] op_sel:[1,1,0] op_sel_hi:[1,0,1] neg_lo:[0,1,0]
	ds_write_b64 v1, v[68:69] offset:26208
	v_pk_mul_f32 v[68:69], v[66:67], v[8:9] op_sel:[0,0] op_sel_hi:[0,1]
	v_pk_fma_f32 v[68:69], v[66:67], v[8:9], v[68:69] op_sel:[1,1,0] op_sel_hi:[1,0,1] neg_lo:[0,1,0]
	v_pk_mul_f32 v[66:67], v[70:71], v[4:5] op_sel:[0,0] op_sel_hi:[0,1]
	v_pk_fma_f32 v[66:67], v[70:71], v[4:5], v[66:67] op_sel:[1,1,0] op_sel_hi:[1,0,1] neg_lo:[0,1,0]
	ds_write_b64 v1, v[66:67] offset:30576
	v_pk_mul_f32 v[66:67], v[64:65], v[2:3] op_sel:[0,0] op_sel_hi:[0,1]
	v_pk_fma_f32 v[66:67], v[64:65], v[2:3], v[66:67] op_sel:[1,1,0] op_sel_hi:[1,0,1] neg_lo:[0,1,0]
	ds_write_b64 v1, v[98:99]
	ds_write_b64 v1, v[90:91] offset:2184
	ds_write_b64 v1, v[88:89] offset:4368
	ds_write_b64 v1, v[74:75] offset:15288
	ds_write_b64 v1, v[72:73] offset:24024
	ds_write_b64 v1, v[68:69] offset:28392
	ds_write_b64 v1, v[66:67] offset:32760
	s_waitcnt lgkmcnt(0)
	s_barrier
	ds_read2_b64 v[64:67], v96 offset1:16
	ds_read2_b64 v[68:71], v96 offset0:32 offset1:48
	ds_read2_b64 v[72:75], v96 offset0:64 offset1:80
	ds_read2_b64 v[76:79], v96 offset0:128 offset1:144
	ds_read2_b64 v[80:83], v96 offset0:96 offset1:112
	ds_read2_b64 v[84:87], v96 offset0:192 offset1:208
	ds_read2_b64 v[88:91], v96 offset0:160 offset1:176
	ds_read2_b64 v[92:95], v96 offset0:224 offset1:240
	s_waitcnt lgkmcnt(4)
	v_pk_add_f32 v[98:99], v[64:65], v[76:77]
	v_pk_add_f32 v[64:65], v[64:65], v[76:77] neg_lo:[0,1] neg_hi:[0,1]
	s_waitcnt lgkmcnt(2)
	v_pk_add_f32 v[76:77], v[72:73], v[84:85]
	v_pk_add_f32 v[72:73], v[72:73], v[84:85] neg_lo:[0,1] neg_hi:[0,1]
	v_pk_add_f32 v[84:85], v[98:99], v[76:77]
	v_pk_add_f32 v[76:77], v[98:99], v[76:77] neg_lo:[0,1] neg_hi:[0,1]
	v_pk_add_f32 v[98:99], v[64:65], v[72:73] op_sel:[0,1] op_sel_hi:[1,0] neg_hi:[0,1]
	v_pk_add_f32 v[64:65], v[64:65], v[72:73] op_sel:[0,1] op_sel_hi:[1,0] neg_lo:[0,1]
	v_pk_add_f32 v[72:73], v[66:67], v[78:79]
	v_pk_add_f32 v[66:67], v[66:67], v[78:79] neg_lo:[0,1] neg_hi:[0,1]
	v_pk_add_f32 v[78:79], v[74:75], v[86:87]
	v_pk_add_f32 v[74:75], v[74:75], v[86:87] neg_lo:[0,1] neg_hi:[0,1]
	v_pk_add_f32 v[86:87], v[72:73], v[78:79]
	v_pk_add_f32 v[72:73], v[72:73], v[78:79] neg_lo:[0,1] neg_hi:[0,1]
	v_pk_add_f32 v[78:79], v[66:67], v[74:75] op_sel:[0,1] op_sel_hi:[1,0] neg_hi:[0,1]
	v_pk_add_f32 v[66:67], v[66:67], v[74:75] op_sel:[0,1] op_sel_hi:[1,0] neg_lo:[0,1]
	s_waitcnt lgkmcnt(1)
	v_pk_add_f32 v[74:75], v[68:69], v[88:89]
	v_pk_add_f32 v[68:69], v[68:69], v[88:89] neg_lo:[0,1] neg_hi:[0,1]
	s_waitcnt lgkmcnt(0)
	v_pk_add_f32 v[88:89], v[80:81], v[92:93]
	v_pk_add_f32 v[80:81], v[80:81], v[92:93] neg_lo:[0,1] neg_hi:[0,1]
	v_pk_add_f32 v[92:93], v[74:75], v[88:89]
	v_pk_add_f32 v[74:75], v[74:75], v[88:89] neg_lo:[0,1] neg_hi:[0,1]
	v_pk_add_f32 v[88:89], v[68:69], v[80:81] op_sel:[0,1] op_sel_hi:[1,0] neg_hi:[0,1]
	v_pk_add_f32 v[68:69], v[68:69], v[80:81] op_sel:[0,1] op_sel_hi:[1,0] neg_lo:[0,1]
	v_pk_add_f32 v[80:81], v[70:71], v[90:91]
	v_pk_add_f32 v[70:71], v[70:71], v[90:91] neg_lo:[0,1] neg_hi:[0,1]
	v_pk_add_f32 v[90:91], v[82:83], v[94:95]
	v_pk_add_f32 v[82:83], v[82:83], v[94:95] neg_lo:[0,1] neg_hi:[0,1]
	v_pk_add_f32 v[94:95], v[80:81], v[90:91]
	v_pk_add_f32 v[80:81], v[80:81], v[90:91] neg_lo:[0,1] neg_hi:[0,1]
	v_pk_add_f32 v[90:91], v[70:71], v[82:83] op_sel:[0,1] op_sel_hi:[1,0] neg_hi:[0,1]
	v_pk_add_f32 v[70:71], v[70:71], v[82:83] op_sel:[0,1] op_sel_hi:[1,0] neg_lo:[0,1]
	v_pk_mul_f32 v[82:83], v[78:79], s[6:7] op_sel:[0,0] op_sel_hi:[0,1]
	v_pk_fma_f32 v[82:83], v[78:79], s[6:7], v[82:83] op_sel:[1,1,0] op_sel_hi:[1,0,1] neg_lo:[0,1,0]
	v_pk_mul_f32 v[78:79], v[66:67], s[10:11] op_sel:[0,0] op_sel_hi:[0,1]
	v_pk_fma_f32 v[78:79], v[66:67], s[10:11], v[78:79] op_sel:[1,1,0] op_sel_hi:[1,0,1] neg_lo:[0,1,0]
	v_pk_add_f32 v[66:67], v[88:89], v[88:89] op_sel:[0,1] op_sel_hi:[1,0] neg_hi:[0,1]
	v_pk_add_f32 v[72:73], v[72:73], v[72:73] op_sel:[0,1] op_sel_hi:[1,0] neg_hi:[0,1]
	s_nop 0
	v_pk_mul_f32 v[88:89], v[90:91], s[10:11] op_sel:[0,0] op_sel_hi:[0,1]
	v_pk_fma_f32 v[88:89], v[90:91], s[10:11], v[88:89] op_sel:[1,1,0] op_sel_hi:[1,0,1] neg_lo:[0,1,0]
	v_pk_mul_f32 v[90:91], v[70:71], s[14:15] op_sel:[0,0] op_sel_hi:[0,1]
	v_pk_fma_f32 v[90:91], v[70:71], s[14:15], v[90:91] op_sel:[1,1,0] op_sel_hi:[1,0,1] neg_lo:[0,1,0]
	v_pk_add_f32 v[70:71], v[84:85], v[92:93]
	v_pk_mul_f32 v[66:67], v[66:67], s[8:9]
	v_pk_add_f32 v[84:85], v[84:85], v[92:93] neg_lo:[0,1] neg_hi:[0,1]
	v_pk_add_f32 v[92:93], v[86:87], v[94:95]
	v_pk_add_f32 v[86:87], v[86:87], v[94:95] neg_lo:[0,1] neg_hi:[0,1]
	v_pk_add_f32 v[68:69], v[68:69], v[68:69] op_sel:[0,1] op_sel_hi:[1,0] neg_lo:[0,1]
	v_pk_add_f32 v[80:81], v[80:81], v[80:81] op_sel:[0,1] op_sel_hi:[1,0] neg_lo:[0,1]
	v_pk_add_f32 v[94:95], v[70:71], v[92:93]
	v_pk_add_f32 v[92:93], v[70:71], v[92:93] neg_lo:[0,1] neg_hi:[0,1]
	v_pk_add_f32 v[100:101], v[84:85], v[86:87] op_sel:[0,1] op_sel_hi:[1,0] neg_hi:[0,1]
	v_pk_add_f32 v[84:85], v[84:85], v[86:87] op_sel:[0,1] op_sel_hi:[1,0] neg_lo:[0,1]
	v_pk_add_f32 v[70:71], v[98:99], v[66:67]
	v_pk_add_f32 v[66:67], v[98:99], v[66:67] neg_lo:[0,1] neg_hi:[0,1]
	v_pk_add_f32 v[86:87], v[82:83], v[88:89]
	v_pk_add_f32 v[82:83], v[82:83], v[88:89] neg_lo:[0,1] neg_hi:[0,1]
	v_pk_mul_f32 v[72:73], v[72:73], s[8:9]
	v_pk_mul_f32 v[68:69], v[68:69], s[12:13]
	v_pk_mul_f32 v[80:81], v[80:81], s[12:13]
	v_pk_add_f32 v[88:89], v[70:71], v[86:87]
	v_pk_add_f32 v[86:87], v[70:71], v[86:87] neg_lo:[0,1] neg_hi:[0,1]
	v_pk_add_f32 v[98:99], v[66:67], v[82:83] op_sel:[0,1] op_sel_hi:[1,0] neg_hi:[0,1]
	v_pk_add_f32 v[82:83], v[66:67], v[82:83] op_sel:[0,1] op_sel_hi:[1,0] neg_lo:[0,1]
	v_pk_add_f32 v[66:67], v[76:77], v[74:75] op_sel:[0,1] op_sel_hi:[1,0] neg_hi:[0,1]
	v_pk_add_f32 v[70:71], v[76:77], v[74:75] op_sel:[0,1] op_sel_hi:[1,0] neg_lo:[0,1]
	v_pk_add_f32 v[74:75], v[72:73], v[80:81]
	v_pk_add_f32 v[72:73], v[72:73], v[80:81] neg_lo:[0,1] neg_hi:[0,1]
	v_pk_add_f32 v[76:77], v[74:75], v[66:67]
	v_pk_add_f32 v[74:75], v[66:67], v[74:75] neg_lo:[0,1] neg_hi:[0,1]
	v_pk_add_f32 v[66:67], v[64:65], v[68:69]
	v_pk_add_f32 v[64:65], v[64:65], v[68:69] neg_lo:[0,1] neg_hi:[0,1]
	v_pk_add_f32 v[68:69], v[78:79], v[90:91]
	v_pk_add_f32 v[80:81], v[70:71], v[72:73] op_sel:[0,1] op_sel_hi:[1,0] neg_hi:[0,1]
	v_pk_add_f32 v[72:73], v[70:71], v[72:73] op_sel:[0,1] op_sel_hi:[1,0] neg_lo:[0,1]
	v_pk_add_f32 v[70:71], v[78:79], v[90:91] neg_lo:[0,1] neg_hi:[0,1]
	v_pk_add_f32 v[78:79], v[66:67], v[68:69]
	v_pk_add_f32 v[90:91], v[66:67], v[68:69] neg_lo:[0,1] neg_hi:[0,1]
	v_mov_b32_e32 v68, v0
	v_pk_add_f32 v[102:103], v[64:65], v[70:71] op_sel:[0,1] op_sel_hi:[1,0] neg_hi:[0,1]
	v_pk_add_f32 v[104:105], v[64:65], v[70:71] op_sel:[0,1] op_sel_hi:[1,0] neg_lo:[0,1]
	s_nop 0
	v_ashrrev_i32_e32 v64, 4, v68
	v_lshlrev_b32_e32 v97, 3, v64
	v_add_u32_e32 v108, 0x8800, v97
	v_and_b32_e32 v68, 15, v68
	ds_read2_b64 v[64:67], v108 offset0:16 offset1:32
	v_mad_u32_u24 v109, v68, s5, v97
	ds_read2_b64 v[68:71], v108 offset0:48 offset1:64
	s_waitcnt lgkmcnt(1)
	v_pk_mul_f32 v[106:107], v[88:89], v[64:65] op_sel:[0,0] op_sel_hi:[0,1]
	v_pk_fma_f32 v[106:107], v[88:89], v[64:65], v[106:107] op_sel:[1,1,0] op_sel_hi:[1,0,1] neg_lo:[0,1,0]
	v_pk_mul_f32 v[88:89], v[76:77], v[66:67] op_sel:[0,0] op_sel_hi:[0,1]
	v_pk_fma_f32 v[88:89], v[76:77], v[66:67], v[88:89] op_sel:[1,1,0] op_sel_hi:[1,0,1] neg_lo:[0,1,0]
	s_waitcnt lgkmcnt(0)
	v_pk_mul_f32 v[76:77], v[78:79], v[68:69] op_sel:[0,0] op_sel_hi:[0,1]
	v_pk_fma_f32 v[76:77], v[78:79], v[68:69], v[76:77] op_sel:[1,1,0] op_sel_hi:[1,0,1] neg_lo:[0,1,0]
	ds_write2_b64 v109, v[88:89], v[76:77] offset0:32 offset1:48
	v_pk_mul_f32 v[76:77], v[100:101], v[70:71] op_sel:[0,0] op_sel_hi:[0,1]
	v_pk_fma_f32 v[76:77], v[100:101], v[70:71], v[76:77] op_sel:[1,1,0] op_sel_hi:[1,0,1] neg_lo:[0,1,0]
	ds_read2_b64 v[64:67], v108 offset0:80 offset1:96
	s_waitcnt lgkmcnt(0)
	v_pk_mul_f32 v[78:79], v[98:99], v[64:65] op_sel:[0,0] op_sel_hi:[0,1]
	v_pk_fma_f32 v[78:79], v[98:99], v[64:65], v[78:79] op_sel:[1,1,0] op_sel_hi:[1,0,1] neg_lo:[0,1,0]
	ds_write2_b64 v109, v[76:77], v[78:79] offset0:64 offset1:80
	v_pk_mul_f32 v[76:77], v[80:81], v[66:67] op_sel:[0,0] op_sel_hi:[0,1]
	v_pk_fma_f32 v[76:77], v[80:81], v[66:67], v[76:77] op_sel:[1,1,0] op_sel_hi:[1,0,1] neg_lo:[0,1,0]
	ds_read2_b64 v[68:71], v108 offset0:112 offset1:128
	ds_read2_b64 v[64:67], v108 offset0:144 offset1:160
	s_waitcnt lgkmcnt(1)
	v_pk_mul_f32 v[78:79], v[102:103], v[68:69] op_sel:[0,0] op_sel_hi:[0,1]
	v_pk_fma_f32 v[78:79], v[102:103], v[68:69], v[78:79] op_sel:[1,1,0] op_sel_hi:[1,0,1] neg_lo:[0,1,0]
	ds_write2_b64 v109, v[76:77], v[78:79] offset0:96 offset1:112
	v_pk_mul_f32 v[76:77], v[92:93], v[70:71] op_sel:[0,0] op_sel_hi:[0,1]
	v_pk_fma_f32 v[76:77], v[92:93], v[70:71], v[76:77] op_sel:[1,1,0] op_sel_hi:[1,0,1] neg_lo:[0,1,0]
	ds_read2_b64 v[68:71], v108 offset0:176 offset1:192
	s_waitcnt lgkmcnt(2)
	v_pk_mul_f32 v[78:79], v[86:87], v[64:65] op_sel:[0,0] op_sel_hi:[0,1]
	v_pk_fma_f32 v[78:79], v[86:87], v[64:65], v[78:79] op_sel:[1,1,0] op_sel_hi:[1,0,1] neg_lo:[0,1,0]
	ds_write2_b64 v109, v[76:77], v[78:79] offset0:128 offset1:144
	v_pk_mul_f32 v[76:77], v[74:75], v[66:67] op_sel:[0,0] op_sel_hi:[0,1]
	v_pk_fma_f32 v[76:77], v[74:75], v[66:67], v[76:77] op_sel:[1,1,0] op_sel_hi:[1,0,1] neg_lo:[0,1,0]
	ds_read2_b64 v[64:67], v108 offset0:208 offset1:224
	s_waitcnt lgkmcnt(2)
	v_pk_mul_f32 v[74:75], v[90:91], v[68:69] op_sel:[0,0] op_sel_hi:[0,1]
	v_pk_fma_f32 v[74:75], v[90:91], v[68:69], v[74:75] op_sel:[1,1,0] op_sel_hi:[1,0,1] neg_lo:[0,1,0]
	ds_write2_b64 v109, v[76:77], v[74:75] offset0:160 offset1:176
	v_pk_mul_f32 v[74:75], v[84:85], v[70:71] op_sel:[0,0] op_sel_hi:[0,1]
	v_pk_fma_f32 v[74:75], v[84:85], v[70:71], v[74:75] op_sel:[1,1,0] op_sel_hi:[1,0,1] neg_lo:[0,1,0]
	s_waitcnt lgkmcnt(1)
	v_pk_mul_f32 v[70:71], v[82:83], v[64:65] op_sel:[0,0] op_sel_hi:[0,1]
	v_pk_fma_f32 v[70:71], v[82:83], v[64:65], v[70:71] op_sel:[1,1,0] op_sel_hi:[1,0,1] neg_lo:[0,1,0]
	v_pk_mul_f32 v[64:65], v[72:73], v[66:67] op_sel:[0,0] op_sel_hi:[0,1]
	v_pk_fma_f32 v[64:65], v[72:73], v[66:67], v[64:65] op_sel:[1,1,0] op_sel_hi:[1,0,1] neg_lo:[0,1,0]
	ds_read_b64 v[68:69], v97 offset:36736
	s_waitcnt lgkmcnt(0)
	v_pk_mul_f32 v[66:67], v[104:105], v[68:69] op_sel:[0,0] op_sel_hi:[0,1]
	v_pk_fma_f32 v[66:67], v[104:105], v[68:69], v[66:67] op_sel:[1,1,0] op_sel_hi:[1,0,1] neg_lo:[0,1,0]
	ds_write2_b64 v109, v[64:65], v[66:67] offset0:224 offset1:240
	v_mov_b32_e32 v64, v0
	ds_write2_b64 v109, v[94:95], v[106:107] offset1:16
	ds_write2_b64 v109, v[74:75], v[70:71] offset0:192 offset1:208
	s_waitcnt lgkmcnt(0)
	s_barrier
	s_nop 0
	v_and_b32_e32 v65, 15, v64
	v_and_b32_e32 v64, 0x1ffffff0, v64
	v_lshlrev_b32_e32 v64, 3, v64
	v_mad_u32_u24 v92, v65, s5, v64
	ds_read2_b64 v[64:67], v92 offset1:1
	ds_read2_b64 v[68:71], v92 offset0:2 offset1:3
	ds_read2_b64 v[72:75], v92 offset0:8 offset1:9
	ds_read2_b64 v[76:79], v92 offset0:4 offset1:5
	ds_read2_b64 v[80:83], v92 offset0:6 offset1:7
	ds_read2_b64 v[84:87], v92 offset0:12 offset1:13
	ds_read2_b64 v[88:91], v92 offset0:10 offset1:11
	ds_read2_b64 v[92:95], v92 offset0:14 offset1:15
	s_waitcnt lgkmcnt(5)
	v_pk_add_f32 v[98:99], v[64:65], v[72:73]
	v_pk_add_f32 v[64:65], v[64:65], v[72:73] neg_lo:[0,1] neg_hi:[0,1]
	s_waitcnt lgkmcnt(2)
	v_pk_add_f32 v[72:73], v[76:77], v[84:85]
	v_pk_add_f32 v[76:77], v[76:77], v[84:85] neg_lo:[0,1] neg_hi:[0,1]
	v_pk_add_f32 v[84:85], v[98:99], v[72:73]
	v_pk_add_f32 v[98:99], v[98:99], v[72:73] neg_lo:[0,1] neg_hi:[0,1]
	v_pk_add_f32 v[100:101], v[64:65], v[76:77] op_sel:[0,1] op_sel_hi:[1,0] neg_hi:[0,1]
	v_pk_add_f32 v[102:103], v[64:65], v[76:77] op_sel:[0,1] op_sel_hi:[1,0] neg_lo:[0,1]
	v_pk_add_f32 v[64:65], v[66:67], v[74:75]
	v_pk_add_f32 v[72:73], v[78:79], v[86:87]
	v_pk_add_f32 v[66:67], v[66:67], v[74:75] neg_lo:[0,1] neg_hi:[0,1]
	v_pk_add_f32 v[74:75], v[78:79], v[86:87] neg_lo:[0,1] neg_hi:[0,1]
	v_pk_add_f32 v[76:77], v[64:65], v[72:73]
	v_pk_add_f32 v[64:65], v[64:65], v[72:73] neg_lo:[0,1] neg_hi:[0,1]
	v_pk_add_f32 v[72:73], v[66:67], v[74:75] op_sel:[0,1] op_sel_hi:[1,0] neg_hi:[0,1]
	v_pk_add_f32 v[66:67], v[66:67], v[74:75] op_sel:[0,1] op_sel_hi:[1,0] neg_lo:[0,1]
	s_waitcnt lgkmcnt(1)
	v_pk_add_f32 v[74:75], v[68:69], v[88:89]
	s_waitcnt lgkmcnt(0)
	v_pk_add_f32 v[78:79], v[80:81], v[92:93]
	v_pk_add_f32 v[64:65], v[64:65], v[64:65] op_sel:[0,1] op_sel_hi:[1,0] neg_hi:[0,1]
	v_pk_add_f32 v[68:69], v[68:69], v[88:89] neg_lo:[0,1] neg_hi:[0,1]
	v_pk_add_f32 v[80:81], v[80:81], v[92:93] neg_lo:[0,1] neg_hi:[0,1]
	v_pk_add_f32 v[86:87], v[74:75], v[78:79]
	v_pk_add_f32 v[78:79], v[74:75], v[78:79] neg_lo:[0,1] neg_hi:[0,1]
	v_pk_add_f32 v[74:75], v[68:69], v[80:81] op_sel:[0,1] op_sel_hi:[1,0] neg_hi:[0,1]
	v_pk_mul_f32 v[92:93], v[64:65], s[8:9]
	v_pk_add_f32 v[68:69], v[68:69], v[80:81] op_sel:[0,1] op_sel_hi:[1,0] neg_lo:[0,1]
	v_pk_add_f32 v[80:81], v[70:71], v[90:91]
	v_pk_add_f32 v[64:65], v[74:75], v[74:75] op_sel:[0,1] op_sel_hi:[1,0] neg_hi:[0,1]
	v_pk_add_f32 v[70:71], v[70:71], v[90:91] neg_lo:[0,1] neg_hi:[0,1]
	v_pk_add_f32 v[88:89], v[82:83], v[94:95]
	v_pk_add_f32 v[82:83], v[82:83], v[94:95] neg_lo:[0,1] neg_hi:[0,1]
	v_pk_mul_f32 v[94:95], v[66:67], s[10:11] op_sel:[0,0] op_sel_hi:[0,1]
	v_pk_fma_f32 v[94:95], v[66:67], s[10:11], v[94:95] op_sel:[1,1,0] op_sel_hi:[1,0,1] neg_lo:[0,1,0]
	v_pk_mul_f32 v[66:67], v[64:65], s[8:9]
	v_pk_add_f32 v[64:65], v[68:69], v[68:69] op_sel:[0,1] op_sel_hi:[1,0] neg_lo:[0,1]
	v_pk_add_f32 v[90:91], v[80:81], v[88:89]
	v_pk_add_f32 v[80:81], v[80:81], v[88:89] neg_lo:[0,1] neg_hi:[0,1]
	v_pk_add_f32 v[88:89], v[70:71], v[82:83] op_sel:[0,1] op_sel_hi:[1,0] neg_hi:[0,1]
	v_pk_add_f32 v[70:71], v[70:71], v[82:83] op_sel:[0,1] op_sel_hi:[1,0] neg_lo:[0,1]
	v_pk_mul_f32 v[104:105], v[64:65], s[12:13]
	v_pk_mul_f32 v[82:83], v[72:73], s[6:7] op_sel:[0,0] op_sel_hi:[0,1]
	v_pk_fma_f32 v[82:83], v[72:73], s[6:7], v[82:83] op_sel:[1,1,0] op_sel_hi:[1,0,1] neg_lo:[0,1,0]
	v_pk_add_f32 v[72:73], v[76:77], v[90:91]
	v_pk_add_f32 v[64:65], v[80:81], v[80:81] op_sel:[0,1] op_sel_hi:[1,0] neg_lo:[0,1]
	v_pk_mul_f32 v[68:69], v[88:89], s[10:11] op_sel:[0,0] op_sel_hi:[0,1]
	v_pk_fma_f32 v[68:69], v[88:89], s[10:11], v[68:69] op_sel:[1,1,0] op_sel_hi:[1,0,1] neg_lo:[0,1,0]
	v_pk_mul_f32 v[108:109], v[70:71], s[14:15] op_sel:[0,0] op_sel_hi:[0,1]
	v_pk_fma_f32 v[108:109], v[70:71], s[14:15], v[108:109] op_sel:[1,1,0] op_sel_hi:[1,0,1] neg_lo:[0,1,0]
	v_pk_add_f32 v[70:71], v[84:85], v[86:87] neg_lo:[0,1] neg_hi:[0,1]
	v_pk_mul_f32 v[106:107], v[64:65], s[12:13]
	v_pk_add_f32 v[64:65], v[84:85], v[86:87]
	v_pk_add_f32 v[74:75], v[76:77], v[90:91] neg_lo:[0,1] neg_hi:[0,1]
	v_pk_add_f32 v[88:89], v[64:65], v[72:73]
	v_pk_add_f32 v[72:73], v[64:65], v[72:73] neg_lo:[0,1] neg_hi:[0,1]
	v_pk_add_f32 v[80:81], v[70:71], v[74:75] op_sel:[0,1] op_sel_hi:[1,0] neg_hi:[0,1]
	v_pk_add_f32 v[64:65], v[70:71], v[74:75] op_sel:[0,1] op_sel_hi:[1,0] neg_lo:[0,1]
	v_pk_add_f32 v[70:71], v[100:101], v[66:67]
	v_pk_add_f32 v[66:67], v[100:101], v[66:67] neg_lo:[0,1] neg_hi:[0,1]
	v_pk_add_f32 v[74:75], v[82:83], v[68:69]
	v_pk_add_f32 v[68:69], v[82:83], v[68:69] neg_lo:[0,1] neg_hi:[0,1]
	v_pk_add_f32 v[90:91], v[70:71], v[74:75]
	v_pk_add_f32 v[74:75], v[70:71], v[74:75] neg_lo:[0,1] neg_hi:[0,1]
	v_pk_add_f32 v[82:83], v[66:67], v[68:69] op_sel:[0,1] op_sel_hi:[1,0] neg_hi:[0,1]
	v_pk_add_f32 v[66:67], v[66:67], v[68:69] op_sel:[0,1] op_sel_hi:[1,0] neg_lo:[0,1]
	v_pk_add_f32 v[68:69], v[98:99], v[78:79] op_sel:[0,1] op_sel_hi:[1,0] neg_hi:[0,1]
	v_pk_add_f32 v[70:71], v[98:99], v[78:79] op_sel:[0,1] op_sel_hi:[1,0] neg_lo:[0,1]
	v_pk_add_f32 v[76:77], v[92:93], v[106:107]
	v_pk_add_f32 v[78:79], v[92:93], v[106:107] neg_lo:[0,1] neg_hi:[0,1]
	v_pk_add_f32 v[92:93], v[76:77], v[68:69]
	v_pk_add_f32 v[76:77], v[68:69], v[76:77] neg_lo:[0,1] neg_hi:[0,1]
	v_pk_add_f32 v[86:87], v[70:71], v[78:79] op_sel:[0,1] op_sel_hi:[1,0] neg_hi:[0,1]
	v_pk_add_f32 v[68:69], v[70:71], v[78:79] op_sel:[0,1] op_sel_hi:[1,0] neg_lo:[0,1]
	v_pk_add_f32 v[70:71], v[102:103], v[104:105]
	v_pk_add_f32 v[98:99], v[102:103], v[104:105] neg_lo:[0,1] neg_hi:[0,1]
	v_pk_add_f32 v[78:79], v[94:95], v[108:109]
	v_pk_add_f32 v[100:101], v[94:95], v[108:109] neg_lo:[0,1] neg_hi:[0,1]
	v_pk_add_f32 v[94:95], v[70:71], v[78:79]
	v_pk_add_f32 v[78:79], v[70:71], v[78:79] neg_lo:[0,1] neg_hi:[0,1]
	v_pk_add_f32 v[84:85], v[98:99], v[100:101] op_sel:[0,1] op_sel_hi:[1,0] neg_hi:[0,1]
	v_pk_add_f32 v[70:71], v[98:99], v[100:101] op_sel:[0,1] op_sel_hi:[1,0] neg_lo:[0,1]
	v_mov_b32_e32 v98, v0
	s_nop 0
	v_and_b32_e32 v97, -16, v98
	v_and_b32_e32 v99, 15, v98
	v_lshlrev_b32_e32 v100, 3, v97
	v_mad_u32_u24 v100, v99, s5, v100
	v_cmp_ne_u32_e32 vcc, 0, v99
	ds_write2_b64 v100, v[88:89], v[90:91] offset1:1
	ds_write2_b64 v100, v[92:93], v[94:95] offset0:2 offset1:3
	ds_write2_b64 v100, v[80:81], v[82:83] offset0:4 offset1:5
	ds_write2_b64 v100, v[86:87], v[84:85] offset0:6 offset1:7
	ds_write2_b64 v100, v[72:73], v[74:75] offset0:8 offset1:9
	ds_write2_b64 v100, v[76:77], v[78:79] offset0:10 offset1:11
	ds_write2_b64 v100, v[64:65], v[66:67] offset0:12 offset1:13
	ds_write2_b64 v100, v[68:69], v[70:71] offset0:14 offset1:15
	s_waitcnt lgkmcnt(0)
	s_barrier
	s_and_saveexec_b64 s[6:7], vcc
	s_xor_b64 s[6:7], exec, s[6:7]
	v_sub_u32_e32 v99, 16, v99
	v_mul_u32_u24_e32 v99, 0x111, v99
	v_sub_u32_e32 v97, v99, v97
	v_add_u32_e32 v100, 0xf0, v97
	s_andn2_saveexec_b64 s[6:7], s[6:7]
	v_sub_u32_e32 v97, 0x100, v98
	v_cmp_lt_u32_e32 vcc, 15, v98
	s_nop 1
	v_cndmask_b32_e32 v100, 1, v97, vcc
	s_or_b64 exec, exec, s[6:7]
	v_mov_b32_e32 v97, 0
	v_lshlrev_b32_e32 v110, 3, v100
	ds_read_b64 v[108:109], v97
	ds_read2_b64 v[100:103], v110 offset0:14 offset1:15
	v_cmp_eq_u32_e32 vcc, 0, v98
	ds_read2_b64 v[104:107], v110 offset0:12 offset1:13
	s_mov_b32 s6, 0x3f6c835e
	s_mov_b32 s7, 0xbec3ef15
	s_waitcnt lgkmcnt(1)
	v_cndmask_b32_e32 v99, v103, v109, vcc
	v_cndmask_b32_e32 v98, v102, v108, vcc
	v_pk_add_f32 v[102:103], v[88:89], v[98:99] neg_hi:[0,1]
	v_pk_add_f32 v[88:89], v[88:89], v[98:99] neg_lo:[0,1]
	s_mov_b32 s9, s8
	v_pk_mul_f32 v[98:99], v[102:103], v[88:89] op_sel:[0,0] op_sel_hi:[0,1]
	v_pk_fma_f32 v[98:99], v[102:103], v[88:89], v[98:99] op_sel:[1,1,0] op_sel_hi:[1,0,1] neg_hi:[0,1,0]
	v_pk_add_f32 v[88:89], v[90:91], v[100:101] neg_hi:[0,1]
	v_pk_add_f32 v[90:91], v[90:91], v[100:101] neg_lo:[0,1]
	s_mov_b32 s14, s11
	v_pk_add_f32 v[62:63], v[62:63], v[98:99] op_sel:[1,0] op_sel_hi:[0,1] neg_lo:[0,1] neg_hi:[1,1]
	v_pk_mul_f32 v[98:99], v[88:89], v[90:91] op_sel:[0,0] op_sel_hi:[0,1]
	v_pk_fma_f32 v[98:99], v[88:89], v[90:91], v[98:99] op_sel:[1,1,0] op_sel_hi:[1,0,1] neg_hi:[0,1,0]
	s_waitcnt lgkmcnt(0)
	v_pk_add_f32 v[88:89], v[92:93], v[106:107] neg_hi:[0,1]
	v_pk_add_f32 v[90:91], v[92:93], v[106:107] neg_lo:[0,1]
	s_mov_b32 s15, s10
	v_pk_mul_f32 v[92:93], v[88:89], v[90:91] op_sel:[0,0] op_sel_hi:[0,1]
	v_pk_fma_f32 v[92:93], v[88:89], v[90:91], v[92:93] op_sel:[1,1,0] op_sel_hi:[1,0,1] neg_hi:[0,1,0]
	v_pk_add_f32 v[60:61], v[60:61], v[98:99] op_sel:[1,0] op_sel_hi:[0,1] neg_lo:[0,1] neg_hi:[1,1]
	ds_read2_b64 v[88:91], v110 offset0:10 offset1:11
	v_pk_add_f32 v[58:59], v[58:59], v[92:93] op_sel:[1,0] op_sel_hi:[0,1] neg_lo:[0,1] neg_hi:[1,1]
	v_pk_add_f32 v[92:93], v[94:95], v[104:105] neg_hi:[0,1]
	v_pk_add_f32 v[94:95], v[94:95], v[104:105] neg_lo:[0,1]
	s_mov_b32 s13, s12
	v_pk_mul_f32 v[98:99], v[92:93], v[94:95] op_sel:[0,0] op_sel_hi:[0,1]
	v_pk_fma_f32 v[98:99], v[92:93], v[94:95], v[98:99] op_sel:[1,1,0] op_sel_hi:[1,0,1] neg_hi:[0,1,0]
	ds_read2_b64 v[92:95], v110 offset0:8 offset1:9
	v_pk_add_f32 v[56:57], v[56:57], v[98:99] op_sel:[1,0] op_sel_hi:[0,1] neg_lo:[0,1] neg_hi:[1,1]
	s_waitcnt lgkmcnt(1)
	v_pk_add_f32 v[98:99], v[80:81], v[90:91] neg_hi:[0,1]
	v_pk_add_f32 v[80:81], v[80:81], v[90:91] neg_lo:[0,1]
	s_add_u32 s2, s2, 0x2000000
	v_pk_mul_f32 v[90:91], v[98:99], v[80:81] op_sel:[0,0] op_sel_hi:[0,1]
	v_pk_fma_f32 v[90:91], v[98:99], v[80:81], v[90:91] op_sel:[1,1,0] op_sel_hi:[1,0,1] neg_hi:[0,1,0]
	v_pk_add_f32 v[80:81], v[82:83], v[88:89] neg_hi:[0,1]
	v_pk_add_f32 v[82:83], v[82:83], v[88:89] neg_lo:[0,1]
	s_addc_u32 s3, s3, 0
	v_pk_mul_f32 v[88:89], v[80:81], v[82:83] op_sel:[0,0] op_sel_hi:[0,1]
	v_pk_fma_f32 v[88:89], v[80:81], v[82:83], v[88:89] op_sel:[1,1,0] op_sel_hi:[1,0,1] neg_hi:[0,1,0]
	s_waitcnt lgkmcnt(0)
	v_pk_add_f32 v[80:81], v[86:87], v[94:95] neg_lo:[0,1]
	v_pk_add_f32 v[54:55], v[54:55], v[90:91] op_sel:[1,0] op_sel_hi:[0,1] neg_lo:[0,1] neg_hi:[1,1]
	s_load_dwordx2 s[0:1], s[0:1], 0x8
	v_pk_add_f32 v[88:89], v[52:53], v[88:89] op_sel:[1,0] op_sel_hi:[0,1] neg_lo:[0,1] neg_hi:[1,1]
	v_pk_add_f32 v[52:53], v[86:87], v[94:95] neg_hi:[0,1]
	s_nop 0
	v_pk_mul_f32 v[82:83], v[52:53], v[80:81] op_sel:[0,0] op_sel_hi:[0,1]
	v_pk_fma_f32 v[82:83], v[52:53], v[80:81], v[82:83] op_sel:[1,1,0] op_sel_hi:[1,0,1] neg_hi:[0,1,0]
	v_pk_add_f32 v[80:81], v[84:85], v[92:93] neg_hi:[0,1]
	s_nop 0
	v_pk_add_f32 v[86:87], v[50:51], v[82:83] op_sel:[1,0] op_sel_hi:[0,1] neg_lo:[0,1] neg_hi:[1,1]
	ds_read2_b64 v[50:53], v110 offset0:6 offset1:7
	v_pk_add_f32 v[82:83], v[84:85], v[92:93] neg_lo:[0,1]
	s_nop 0
	v_pk_mul_f32 v[84:85], v[80:81], v[82:83] op_sel:[0,0] op_sel_hi:[0,1]
	v_pk_fma_f32 v[84:85], v[80:81], v[82:83], v[84:85] op_sel:[1,1,0] op_sel_hi:[1,0,1] neg_hi:[0,1,0]
	ds_read2_b64 v[80:83], v110 offset0:4 offset1:5
	v_pk_add_f32 v[84:85], v[48:49], v[84:85] op_sel:[1,0] op_sel_hi:[0,1] neg_lo:[0,1] neg_hi:[1,1]
	s_waitcnt lgkmcnt(0)
	v_pk_add_f32 v[48:49], v[72:73], v[52:53] neg_hi:[0,1]
	v_pk_add_f32 v[52:53], v[72:73], v[52:53] neg_lo:[0,1]
	s_nop 0
	v_pk_mul_f32 v[72:73], v[48:49], v[52:53] op_sel:[0,0] op_sel_hi:[0,1]
	v_pk_fma_f32 v[72:73], v[48:49], v[52:53], v[72:73] op_sel:[1,1,0] op_sel_hi:[1,0,1] neg_hi:[0,1,0]
	v_pk_add_f32 v[48:49], v[74:75], v[50:51] neg_lo:[0,1]
	s_nop 0
	v_pk_add_f32 v[52:53], v[46:47], v[72:73] op_sel:[1,0] op_sel_hi:[0,1] neg_lo:[0,1] neg_hi:[1,1]
	v_pk_add_f32 v[46:47], v[74:75], v[50:51] neg_hi:[0,1]
	s_nop 0
	v_pk_mul_f32 v[50:51], v[46:47], v[48:49] op_sel:[0,0] op_sel_hi:[0,1]
	v_pk_fma_f32 v[50:51], v[46:47], v[48:49], v[50:51] op_sel:[1,1,0] op_sel_hi:[1,0,1] neg_hi:[0,1,0]
	v_pk_add_f32 v[46:47], v[76:77], v[82:83] neg_lo:[0,1]
	s_nop 0
	v_pk_add_f32 v[50:51], v[44:45], v[50:51] op_sel:[1,0] op_sel_hi:[0,1] neg_lo:[0,1] neg_hi:[1,1]
	v_pk_add_f32 v[44:45], v[76:77], v[82:83] neg_hi:[0,1]
	s_nop 0
	v_pk_mul_f32 v[48:49], v[44:45], v[46:47] op_sel:[0,0] op_sel_hi:[0,1]
	v_pk_fma_f32 v[48:49], v[44:45], v[46:47], v[48:49] op_sel:[1,1,0] op_sel_hi:[1,0,1] neg_hi:[0,1,0]
	v_pk_add_f32 v[46:47], v[78:79], v[80:81] neg_hi:[0,1]
	s_nop 0
	v_pk_add_f32 v[72:73], v[42:43], v[48:49] op_sel:[1,0] op_sel_hi:[0,1] neg_lo:[0,1] neg_hi:[1,1]
	ds_read2_b64 v[42:45], v110 offset0:2 offset1:3
	v_pk_add_f32 v[48:49], v[78:79], v[80:81] neg_lo:[0,1]
	s_nop 0
	v_pk_mul_f32 v[74:75], v[46:47], v[48:49] op_sel:[0,0] op_sel_hi:[0,1]
	v_pk_fma_f32 v[74:75], v[46:47], v[48:49], v[74:75] op_sel:[1,1,0] op_sel_hi:[1,0,1] neg_hi:[0,1,0]
	ds_read2_b64 v[46:49], v110 offset1:1
	v_pk_add_f32 v[40:41], v[40:41], v[74:75] op_sel:[1,0] op_sel_hi:[0,1] neg_lo:[0,1] neg_hi:[1,1]
	s_waitcnt lgkmcnt(1)
	v_pk_add_f32 v[74:75], v[64:65], v[44:45] neg_hi:[0,1]
	v_pk_add_f32 v[44:45], v[64:65], v[44:45] neg_lo:[0,1]
	s_waitcnt lgkmcnt(0)
	v_pk_mul_f32 v[64:65], v[74:75], v[44:45] op_sel:[0,0] op_sel_hi:[0,1]
	v_pk_fma_f32 v[64:65], v[74:75], v[44:45], v[64:65] op_sel:[1,1,0] op_sel_hi:[1,0,1] neg_hi:[0,1,0]
	v_pk_add_f32 v[44:45], v[66:67], v[42:43] neg_hi:[0,1]
	v_pk_add_f32 v[42:43], v[66:67], v[42:43] neg_lo:[0,1]
	s_barrier
	v_pk_add_f32 v[38:39], v[38:39], v[64:65] op_sel:[1,0] op_sel_hi:[0,1] neg_lo:[0,1] neg_hi:[1,1]
	v_pk_mul_f32 v[64:65], v[44:45], v[42:43] op_sel:[0,0] op_sel_hi:[0,1]
	v_pk_fma_f32 v[64:65], v[44:45], v[42:43], v[64:65] op_sel:[1,1,0] op_sel_hi:[1,0,1] neg_hi:[0,1,0]
	v_pk_add_f32 v[42:43], v[68:69], v[48:49] neg_hi:[0,1]
	v_pk_add_f32 v[44:45], v[68:69], v[48:49] neg_lo:[0,1]
	s_nop 0
	v_pk_mul_f32 v[48:49], v[42:43], v[44:45] op_sel:[0,0] op_sel_hi:[0,1]
	v_pk_fma_f32 v[48:49], v[42:43], v[44:45], v[48:49] op_sel:[1,1,0] op_sel_hi:[1,0,1] neg_hi:[0,1,0]
	v_pk_add_f32 v[42:43], v[70:71], v[46:47] neg_hi:[0,1]
	v_pk_add_f32 v[44:45], v[70:71], v[46:47] neg_lo:[0,1]
	v_pk_add_f32 v[36:37], v[36:37], v[64:65] op_sel:[1,0] op_sel_hi:[0,1] neg_lo:[0,1] neg_hi:[1,1]
	s_nop 0
	v_pk_mul_f32 v[46:47], v[42:43], v[44:45] op_sel:[0,0] op_sel_hi:[0,1]
	v_pk_fma_f32 v[46:47], v[42:43], v[44:45], v[46:47] op_sel:[1,1,0] op_sel_hi:[1,0,1] neg_hi:[0,1,0]
	v_pk_add_f32 v[42:43], v[62:63], v[52:53]
	v_pk_add_f32 v[32:33], v[32:33], v[46:47] op_sel:[1,0] op_sel_hi:[0,1] neg_lo:[0,1] neg_hi:[1,1]
	v_pk_add_f32 v[44:45], v[62:63], v[52:53] neg_lo:[0,1] neg_hi:[0,1]
	v_pk_add_f32 v[46:47], v[54:55], v[38:39]
	v_pk_add_f32 v[38:39], v[54:55], v[38:39] neg_lo:[0,1] neg_hi:[0,1]
	v_pk_add_f32 v[34:35], v[34:35], v[48:49] op_sel:[1,0] op_sel_hi:[0,1] neg_lo:[0,1] neg_hi:[1,1]
	v_pk_add_f32 v[48:49], v[42:43], v[46:47]
	v_pk_add_f32 v[42:43], v[42:43], v[46:47] neg_lo:[0,1] neg_hi:[0,1]
	v_pk_add_f32 v[46:47], v[44:45], v[38:39] op_sel:[0,1] op_sel_hi:[1,0] neg_hi:[0,1]
	v_pk_add_f32 v[38:39], v[44:45], v[38:39] op_sel:[0,1] op_sel_hi:[1,0] neg_lo:[0,1]
	v_pk_add_f32 v[44:45], v[60:61], v[50:51]
	v_pk_add_f32 v[50:51], v[60:61], v[50:51] neg_lo:[0,1] neg_hi:[0,1]
	v_pk_add_f32 v[52:53], v[88:89], v[36:37]
	v_pk_add_f32 v[36:37], v[88:89], v[36:37] neg_lo:[0,1] neg_hi:[0,1]
	v_pk_add_f32 v[54:55], v[44:45], v[52:53]
	v_pk_add_f32 v[44:45], v[44:45], v[52:53] neg_lo:[0,1] neg_hi:[0,1]
	v_pk_add_f32 v[52:53], v[50:51], v[36:37] op_sel:[0,1] op_sel_hi:[1,0] neg_hi:[0,1]
	v_pk_add_f32 v[36:37], v[50:51], v[36:37] op_sel:[0,1] op_sel_hi:[1,0] neg_lo:[0,1]
	v_pk_add_f32 v[50:51], v[58:59], v[72:73]
	v_pk_add_f32 v[58:59], v[58:59], v[72:73] neg_lo:[0,1] neg_hi:[0,1]
	v_pk_add_f32 v[60:61], v[86:87], v[34:35]
	v_pk_add_f32 v[34:35], v[86:87], v[34:35] neg_lo:[0,1] neg_hi:[0,1]
	v_pk_add_f32 v[62:63], v[50:51], v[60:61]
	v_pk_add_f32 v[50:51], v[50:51], v[60:61] neg_lo:[0,1] neg_hi:[0,1]
	v_pk_add_f32 v[60:61], v[58:59], v[34:35] op_sel:[0,1] op_sel_hi:[1,0] neg_hi:[0,1]
	v_pk_add_f32 v[34:35], v[58:59], v[34:35] op_sel:[0,1] op_sel_hi:[1,0] neg_lo:[0,1]
	v_pk_add_f32 v[58:59], v[56:57], v[40:41]
	v_pk_add_f32 v[40:41], v[56:57], v[40:41] neg_lo:[0,1] neg_hi:[0,1]
	v_pk_add_f32 v[56:57], v[84:85], v[32:33]
	v_pk_add_f32 v[32:33], v[84:85], v[32:33] neg_lo:[0,1] neg_hi:[0,1]
	v_pk_add_f32 v[64:65], v[58:59], v[56:57]
	v_pk_add_f32 v[56:57], v[58:59], v[56:57] neg_lo:[0,1] neg_hi:[0,1]
	v_pk_add_f32 v[58:59], v[40:41], v[32:33] op_sel:[0,1] op_sel_hi:[1,0] neg_hi:[0,1]
	v_pk_add_f32 v[32:33], v[40:41], v[32:33] op_sel:[0,1] op_sel_hi:[1,0] neg_lo:[0,1]
	v_pk_mul_f32 v[40:41], v[52:53], s[6:7] op_sel:[0,0] op_sel_hi:[0,1]
	v_pk_fma_f32 v[40:41], v[52:53], s[6:7], v[40:41] op_sel:[1,1,0] op_sel_hi:[1,0,1] neg_lo:[0,1,0]
	v_pk_mul_f32 v[52:53], v[36:37], s[10:11] op_sel:[0,0] op_sel_hi:[0,1]
	v_pk_fma_f32 v[52:53], v[36:37], s[10:11], v[52:53] op_sel:[1,1,0] op_sel_hi:[1,0,1] neg_lo:[0,1,0]
	v_pk_add_f32 v[36:37], v[60:61], v[60:61] op_sel:[0,1] op_sel_hi:[1,0] neg_hi:[0,1]
	v_pk_add_f32 v[44:45], v[44:45], v[44:45] op_sel:[0,1] op_sel_hi:[1,0] neg_hi:[0,1]
	s_nop 0
	v_pk_mul_f32 v[60:61], v[58:59], s[10:11] op_sel:[0,0] op_sel_hi:[0,1]
	v_pk_fma_f32 v[60:61], v[58:59], s[10:11], v[60:61] op_sel:[1,1,0] op_sel_hi:[1,0,1] neg_lo:[0,1,0]
	v_pk_mul_f32 v[58:59], v[32:33], s[14:15] op_sel:[0,0] op_sel_hi:[0,1]
	v_pk_fma_f32 v[58:59], v[32:33], s[14:15], v[58:59] op_sel:[1,1,0] op_sel_hi:[1,0,1] neg_lo:[0,1,0]
	v_pk_add_f32 v[32:33], v[48:49], v[62:63]
	v_pk_mul_f32 v[36:37], v[36:37], s[8:9]
	v_pk_add_f32 v[48:49], v[48:49], v[62:63] neg_lo:[0,1] neg_hi:[0,1]
	v_pk_add_f32 v[62:63], v[54:55], v[64:65]
	v_pk_add_f32 v[54:55], v[54:55], v[64:65] neg_lo:[0,1] neg_hi:[0,1]
	v_pk_mul_f32 v[44:45], v[44:45], s[8:9]
	v_pk_add_f32 v[34:35], v[34:35], v[34:35] op_sel:[0,1] op_sel_hi:[1,0] neg_lo:[0,1]
	v_pk_add_f32 v[56:57], v[56:57], v[56:57] op_sel:[0,1] op_sel_hi:[1,0] neg_lo:[0,1]
	v_pk_add_f32 v[64:65], v[32:33], v[62:63]
	v_pk_add_f32 v[32:33], v[32:33], v[62:63] neg_lo:[0,1] neg_hi:[0,1]
	v_pk_add_f32 v[62:63], v[48:49], v[54:55] op_sel:[0,1] op_sel_hi:[1,0] neg_hi:[0,1]
	v_pk_add_f32 v[48:49], v[48:49], v[54:55] op_sel:[0,1] op_sel_hi:[1,0] neg_lo:[0,1]
	v_pk_add_f32 v[54:55], v[46:47], v[36:37]
	v_pk_add_f32 v[36:37], v[46:47], v[36:37] neg_lo:[0,1] neg_hi:[0,1]
	v_pk_add_f32 v[46:47], v[40:41], v[60:61]
	v_pk_add_f32 v[40:41], v[40:41], v[60:61] neg_lo:[0,1] neg_hi:[0,1]
	v_pk_mul_f32 v[34:35], v[34:35], s[12:13]
	v_pk_mul_f32 v[56:57], v[56:57], s[12:13]
	v_pk_add_f32 v[60:61], v[54:55], v[46:47]
	v_pk_add_f32 v[46:47], v[54:55], v[46:47] neg_lo:[0,1] neg_hi:[0,1]
	v_pk_add_f32 v[54:55], v[36:37], v[40:41] op_sel:[0,1] op_sel_hi:[1,0] neg_hi:[0,1]
	v_pk_add_f32 v[36:37], v[36:37], v[40:41] op_sel:[0,1] op_sel_hi:[1,0] neg_lo:[0,1]
	v_pk_add_f32 v[40:41], v[42:43], v[50:51] op_sel:[0,1] op_sel_hi:[1,0] neg_hi:[0,1]
	v_pk_add_f32 v[42:43], v[42:43], v[50:51] op_sel:[0,1] op_sel_hi:[1,0] neg_lo:[0,1]
	v_pk_add_f32 v[50:51], v[44:45], v[56:57]
	v_pk_add_f32 v[44:45], v[44:45], v[56:57] neg_lo:[0,1] neg_hi:[0,1]
	v_pk_add_f32 v[56:57], v[50:51], v[40:41]
	v_pk_add_f32 v[40:41], v[40:41], v[50:51] neg_lo:[0,1] neg_hi:[0,1]
	v_pk_add_f32 v[50:51], v[42:43], v[44:45] op_sel:[0,1] op_sel_hi:[1,0] neg_hi:[0,1]
	v_pk_add_f32 v[42:43], v[42:43], v[44:45] op_sel:[0,1] op_sel_hi:[1,0] neg_lo:[0,1]
	v_pk_add_f32 v[44:45], v[38:39], v[34:35]
	v_pk_add_f32 v[34:35], v[38:39], v[34:35] neg_lo:[0,1] neg_hi:[0,1]
	v_pk_add_f32 v[38:39], v[52:53], v[58:59]
	v_pk_add_f32 v[52:53], v[52:53], v[58:59] neg_lo:[0,1] neg_hi:[0,1]
	v_pk_add_f32 v[58:59], v[44:45], v[38:39]
	v_pk_add_f32 v[38:39], v[44:45], v[38:39] neg_lo:[0,1] neg_hi:[0,1]
	v_pk_add_f32 v[44:45], v[34:35], v[52:53] op_sel:[0,1] op_sel_hi:[1,0] neg_hi:[0,1]
	v_pk_add_f32 v[34:35], v[34:35], v[52:53] op_sel:[0,1] op_sel_hi:[1,0] neg_lo:[0,1]
	v_pk_mul_f32 v[52:53], v[60:61], v[30:31] op_sel:[0,0] op_sel_hi:[0,1]
	v_pk_fma_f32 v[52:53], v[60:61], v[30:31], v[52:53] op_sel:[1,1,0] op_sel_hi:[1,0,1] neg_lo:[0,1,0]
	v_pk_mul_f32 v[30:31], v[56:57], v[28:29] op_sel:[0,0] op_sel_hi:[0,1]
	v_pk_fma_f32 v[30:31], v[56:57], v[28:29], v[30:31] op_sel:[1,1,0] op_sel_hi:[1,0,1] neg_lo:[0,1,0]
	v_pk_mul_f32 v[28:29], v[58:59], v[26:27] op_sel:[0,0] op_sel_hi:[0,1]
	v_pk_fma_f32 v[28:29], v[58:59], v[26:27], v[28:29] op_sel:[1,1,0] op_sel_hi:[1,0,1] neg_lo:[0,1,0]
	v_pk_mul_f32 v[26:27], v[62:63], v[24:25] op_sel:[0,0] op_sel_hi:[0,1]
	v_pk_fma_f32 v[26:27], v[62:63], v[24:25], v[26:27] op_sel:[1,1,0] op_sel_hi:[1,0,1] neg_lo:[0,1,0]
	v_pk_mul_f32 v[24:25], v[54:55], v[20:21] op_sel:[0,0] op_sel_hi:[0,1]
	v_pk_fma_f32 v[24:25], v[54:55], v[20:21], v[24:25] op_sel:[1,1,0] op_sel_hi:[1,0,1] neg_lo:[0,1,0]
	v_pk_mul_f32 v[20:21], v[50:51], v[16:17] op_sel:[0,0] op_sel_hi:[0,1]
	v_pk_fma_f32 v[20:21], v[50:51], v[16:17], v[20:21] op_sel:[1,1,0] op_sel_hi:[1,0,1] neg_lo:[0,1,0]
	s_nop 0
	v_pk_mul_f32 v[16:17], v[44:45], v[10:11] op_sel:[0,0] op_sel_hi:[0,1]
	v_pk_fma_f32 v[16:17], v[44:45], v[10:11], v[16:17] op_sel:[1,1,0] op_sel_hi:[1,0,1] neg_lo:[0,1,0]
	v_pk_mul_f32 v[10:11], v[32:33], v[22:23] op_sel:[0,0] op_sel_hi:[0,1]
	v_pk_fma_f32 v[10:11], v[32:33], v[22:23], v[10:11] op_sel:[1,1,0] op_sel_hi:[1,0,1] neg_lo:[0,1,0]
	ds_write_b64 v1, v[10:11] offset:17472
	v_pk_mul_f32 v[10:11], v[46:47], v[18:19] op_sel:[0,0] op_sel_hi:[0,1]
	v_pk_fma_f32 v[10:11], v[46:47], v[18:19], v[10:11] op_sel:[1,1,0] op_sel_hi:[1,0,1] neg_lo:[0,1,0]
	ds_write_b64 v1, v[10:11] offset:19656
	v_pk_mul_f32 v[10:11], v[40:41], v[12:13] op_sel:[0,0] op_sel_hi:[0,1]
	v_pk_fma_f32 v[10:11], v[40:41], v[12:13], v[10:11] op_sel:[1,1,0] op_sel_hi:[1,0,1] neg_lo:[0,1,0]
	ds_write_b64 v1, v[10:11] offset:21840
	v_pk_mul_f32 v[10:11], v[38:39], v[14:15] op_sel:[0,0] op_sel_hi:[0,1]
	v_pk_fma_f32 v[10:11], v[38:39], v[14:15], v[10:11] op_sel:[1,1,0] op_sel_hi:[1,0,1] neg_lo:[0,1,0]
	ds_write_b64 v1, v[10:11] offset:24024
	v_pk_mul_f32 v[10:11], v[48:49], v[6:7] op_sel:[0,0] op_sel_hi:[0,1]
	v_pk_fma_f32 v[10:11], v[48:49], v[6:7], v[10:11] op_sel:[1,1,0] op_sel_hi:[1,0,1] neg_lo:[0,1,0]
	v_pk_mul_f32 v[6:7], v[36:37], v[8:9] op_sel:[0,0] op_sel_hi:[0,1]
	v_pk_fma_f32 v[6:7], v[36:37], v[8:9], v[6:7] op_sel:[1,1,0] op_sel_hi:[1,0,1] neg_lo:[0,1,0]
	ds_write_b64 v1, v[6:7] offset:28392
	v_pk_mul_f32 v[6:7], v[42:43], v[4:5] op_sel:[0,0] op_sel_hi:[0,1]
	v_pk_fma_f32 v[6:7], v[42:43], v[4:5], v[6:7] op_sel:[1,1,0] op_sel_hi:[1,0,1] neg_lo:[0,1,0]
	v_pk_mul_f32 v[4:5], v[34:35], v[2:3] op_sel:[0,0] op_sel_hi:[0,1]
	v_pk_fma_f32 v[4:5], v[34:35], v[2:3], v[4:5] op_sel:[1,1,0] op_sel_hi:[1,0,1] neg_lo:[0,1,0]
	ds_write_b64 v1, v[64:65]
	ds_write_b64 v1, v[52:53] offset:2184
	ds_write_b64 v1, v[30:31] offset:4368
	ds_write_b64 v1, v[28:29] offset:6552
	ds_write_b64 v1, v[26:27] offset:8736
	ds_write_b64 v1, v[24:25] offset:10920
	ds_write_b64 v1, v[20:21] offset:13104
	ds_write_b64 v1, v[16:17] offset:15288
	ds_write_b64 v1, v[10:11] offset:26208
	ds_write_b64 v1, v[6:7] offset:30576
	ds_write_b64 v1, v[4:5] offset:32760
	s_waitcnt lgkmcnt(0)
	s_barrier
	ds_read2_b64 v[2:5], v96 offset1:16
	ds_read2_b64 v[6:9], v96 offset0:32 offset1:48
	ds_read2_b64 v[10:13], v96 offset0:64 offset1:80
	ds_read2_b64 v[14:17], v96 offset0:128 offset1:144
	ds_read2_b64 v[18:21], v96 offset0:96 offset1:112
	ds_read2_b64 v[22:25], v96 offset0:192 offset1:208
	ds_read2_b64 v[26:29], v96 offset0:160 offset1:176
	ds_read2_b64 v[30:33], v96 offset0:224 offset1:240
	s_waitcnt lgkmcnt(4)
	v_pk_add_f32 v[34:35], v[2:3], v[14:15]
	v_pk_add_f32 v[2:3], v[2:3], v[14:15] neg_lo:[0,1] neg_hi:[0,1]
	s_waitcnt lgkmcnt(2)
	v_pk_add_f32 v[14:15], v[10:11], v[22:23]
	v_pk_add_f32 v[10:11], v[10:11], v[22:23] neg_lo:[0,1] neg_hi:[0,1]
	v_pk_add_f32 v[22:23], v[34:35], v[14:15]
	v_pk_add_f32 v[14:15], v[34:35], v[14:15] neg_lo:[0,1] neg_hi:[0,1]
	v_pk_add_f32 v[34:35], v[2:3], v[10:11] op_sel:[0,1] op_sel_hi:[1,0] neg_hi:[0,1]
	v_pk_add_f32 v[2:3], v[2:3], v[10:11] op_sel:[0,1] op_sel_hi:[1,0] neg_lo:[0,1]
	v_pk_add_f32 v[10:11], v[4:5], v[16:17]
	v_pk_add_f32 v[4:5], v[4:5], v[16:17] neg_lo:[0,1] neg_hi:[0,1]
	v_pk_add_f32 v[16:17], v[12:13], v[24:25]
	v_pk_add_f32 v[12:13], v[12:13], v[24:25] neg_lo:[0,1] neg_hi:[0,1]
	v_pk_add_f32 v[24:25], v[10:11], v[16:17]
	v_pk_add_f32 v[10:11], v[10:11], v[16:17] neg_lo:[0,1] neg_hi:[0,1]
	v_pk_add_f32 v[16:17], v[4:5], v[12:13] op_sel:[0,1] op_sel_hi:[1,0] neg_hi:[0,1]
	v_pk_add_f32 v[4:5], v[4:5], v[12:13] op_sel:[0,1] op_sel_hi:[1,0] neg_lo:[0,1]
	s_waitcnt lgkmcnt(1)
	v_pk_add_f32 v[12:13], v[6:7], v[26:27]
	v_pk_add_f32 v[6:7], v[6:7], v[26:27] neg_lo:[0,1] neg_hi:[0,1]
	s_waitcnt lgkmcnt(0)
	v_pk_add_f32 v[26:27], v[18:19], v[30:31]
	v_pk_add_f32 v[18:19], v[18:19], v[30:31] neg_lo:[0,1] neg_hi:[0,1]
	v_pk_add_f32 v[30:31], v[12:13], v[26:27]
	v_pk_add_f32 v[12:13], v[12:13], v[26:27] neg_lo:[0,1] neg_hi:[0,1]
	v_pk_add_f32 v[26:27], v[6:7], v[18:19] op_sel:[0,1] op_sel_hi:[1,0] neg_hi:[0,1]
	v_pk_add_f32 v[6:7], v[6:7], v[18:19] op_sel:[0,1] op_sel_hi:[1,0] neg_lo:[0,1]
	v_pk_add_f32 v[18:19], v[8:9], v[28:29]
	v_pk_add_f32 v[8:9], v[8:9], v[28:29] neg_lo:[0,1] neg_hi:[0,1]
	v_pk_add_f32 v[28:29], v[20:21], v[32:33]
	v_pk_add_f32 v[20:21], v[20:21], v[32:33] neg_lo:[0,1] neg_hi:[0,1]
	v_pk_add_f32 v[32:33], v[18:19], v[28:29]
	v_pk_add_f32 v[18:19], v[18:19], v[28:29] neg_lo:[0,1] neg_hi:[0,1]
	v_pk_add_f32 v[28:29], v[8:9], v[20:21] op_sel:[0,1] op_sel_hi:[1,0] neg_hi:[0,1]
	v_pk_add_f32 v[8:9], v[8:9], v[20:21] op_sel:[0,1] op_sel_hi:[1,0] neg_lo:[0,1]
	v_pk_mul_f32 v[20:21], v[16:17], s[6:7] op_sel:[0,0] op_sel_hi:[0,1]
	v_pk_fma_f32 v[20:21], v[16:17], s[6:7], v[20:21] op_sel:[1,1,0] op_sel_hi:[1,0,1] neg_lo:[0,1,0]
	v_pk_mul_f32 v[16:17], v[4:5], s[10:11] op_sel:[0,0] op_sel_hi:[0,1]
	v_pk_fma_f32 v[16:17], v[4:5], s[10:11], v[16:17] op_sel:[1,1,0] op_sel_hi:[1,0,1] neg_lo:[0,1,0]
	v_pk_add_f32 v[4:5], v[26:27], v[26:27] op_sel:[0,1] op_sel_hi:[1,0] neg_hi:[0,1]
	v_pk_add_f32 v[10:11], v[10:11], v[10:11] op_sel:[0,1] op_sel_hi:[1,0] neg_hi:[0,1]
	s_nop 0
	v_pk_mul_f32 v[26:27], v[28:29], s[10:11] op_sel:[0,0] op_sel_hi:[0,1]
	v_pk_fma_f32 v[26:27], v[28:29], s[10:11], v[26:27] op_sel:[1,1,0] op_sel_hi:[1,0,1] neg_lo:[0,1,0]
	v_pk_mul_f32 v[28:29], v[8:9], s[14:15] op_sel:[0,0] op_sel_hi:[0,1]
	v_pk_fma_f32 v[28:29], v[8:9], s[14:15], v[28:29] op_sel:[1,1,0] op_sel_hi:[1,0,1] neg_lo:[0,1,0]
	v_pk_add_f32 v[8:9], v[22:23], v[30:31]
	v_pk_mul_f32 v[4:5], v[4:5], s[8:9]
	v_pk_add_f32 v[22:23], v[22:23], v[30:31] neg_lo:[0,1] neg_hi:[0,1]
	v_pk_add_f32 v[30:31], v[24:25], v[32:33]
	v_pk_add_f32 v[24:25], v[24:25], v[32:33] neg_lo:[0,1] neg_hi:[0,1]
	v_pk_add_f32 v[18:19], v[18:19], v[18:19] op_sel:[0,1] op_sel_hi:[1,0] neg_lo:[0,1]
	v_pk_add_f32 v[32:33], v[8:9], v[30:31]
	v_pk_add_f32 v[30:31], v[8:9], v[30:31] neg_lo:[0,1] neg_hi:[0,1]
	v_pk_add_f32 v[36:37], v[22:23], v[24:25] op_sel:[0,1] op_sel_hi:[1,0] neg_hi:[0,1]
	v_pk_add_f32 v[22:23], v[22:23], v[24:25] op_sel:[0,1] op_sel_hi:[1,0] neg_lo:[0,1]
	v_pk_add_f32 v[8:9], v[34:35], v[4:5]
	v_pk_add_f32 v[4:5], v[34:35], v[4:5] neg_lo:[0,1] neg_hi:[0,1]
	v_pk_add_f32 v[24:25], v[20:21], v[26:27]
	v_pk_add_f32 v[20:21], v[20:21], v[26:27] neg_lo:[0,1] neg_hi:[0,1]
	v_pk_mul_f32 v[10:11], v[10:11], s[8:9]
	v_pk_add_f32 v[6:7], v[6:7], v[6:7] op_sel:[0,1] op_sel_hi:[1,0] neg_lo:[0,1]
	v_pk_mul_f32 v[18:19], v[18:19], s[12:13]
	v_pk_add_f32 v[26:27], v[8:9], v[24:25]
	v_pk_add_f32 v[24:25], v[8:9], v[24:25] neg_lo:[0,1] neg_hi:[0,1]
	v_pk_add_f32 v[34:35], v[4:5], v[20:21] op_sel:[0,1] op_sel_hi:[1,0] neg_hi:[0,1]
	v_pk_add_f32 v[20:21], v[4:5], v[20:21] op_sel:[0,1] op_sel_hi:[1,0] neg_lo:[0,1]
	v_pk_add_f32 v[4:5], v[14:15], v[12:13] op_sel:[0,1] op_sel_hi:[1,0] neg_hi:[0,1]
	v_pk_add_f32 v[8:9], v[14:15], v[12:13] op_sel:[0,1] op_sel_hi:[1,0] neg_lo:[0,1]
	v_pk_add_f32 v[12:13], v[10:11], v[18:19]
	v_pk_mul_f32 v[6:7], v[6:7], s[12:13]
	v_pk_add_f32 v[10:11], v[10:11], v[18:19] neg_lo:[0,1] neg_hi:[0,1]
	v_pk_add_f32 v[14:15], v[12:13], v[4:5]
	v_pk_add_f32 v[12:13], v[4:5], v[12:13] neg_lo:[0,1] neg_hi:[0,1]
	v_pk_add_f32 v[4:5], v[2:3], v[6:7]
	v_pk_add_f32 v[2:3], v[2:3], v[6:7] neg_lo:[0,1] neg_hi:[0,1]
	v_mov_b32_e32 v1, v0
	v_pk_add_f32 v[18:19], v[8:9], v[10:11] op_sel:[0,1] op_sel_hi:[1,0] neg_hi:[0,1]
	v_pk_add_f32 v[10:11], v[8:9], v[10:11] op_sel:[0,1] op_sel_hi:[1,0] neg_lo:[0,1]
	v_pk_add_f32 v[8:9], v[16:17], v[28:29] neg_lo:[0,1] neg_hi:[0,1]
	v_pk_add_f32 v[6:7], v[16:17], v[28:29]
	v_pk_add_f32 v[38:39], v[2:3], v[8:9] op_sel:[0,1] op_sel_hi:[1,0] neg_hi:[0,1]
	v_pk_add_f32 v[40:41], v[2:3], v[8:9] op_sel:[0,1] op_sel_hi:[1,0] neg_lo:[0,1]
	v_ashrrev_i32_e32 v2, 4, v1
	v_lshlrev_b32_e32 v44, 3, v2
	v_add_u32_e32 v45, 0x8800, v44
	v_and_b32_e32 v1, 15, v1
	v_pk_add_f32 v[16:17], v[4:5], v[6:7]
	v_pk_add_f32 v[28:29], v[4:5], v[6:7] neg_lo:[0,1] neg_hi:[0,1]
	ds_read2_b64 v[2:5], v45 offset0:16 offset1:32
	v_mad_u32_u24 v1, v1, s5, v44
	ds_read2_b64 v[6:9], v45 offset0:48 offset1:64
	s_waitcnt lgkmcnt(1)
	v_pk_mul_f32 v[42:43], v[26:27], v[2:3] op_sel:[0,0] op_sel_hi:[0,1]
	v_pk_fma_f32 v[42:43], v[26:27], v[2:3], v[42:43] op_sel:[1,1,0] op_sel_hi:[1,0,1] neg_lo:[0,1,0]
	v_pk_mul_f32 v[26:27], v[14:15], v[4:5] op_sel:[0,0] op_sel_hi:[0,1]
	v_pk_fma_f32 v[26:27], v[14:15], v[4:5], v[26:27] op_sel:[1,1,0] op_sel_hi:[1,0,1] neg_lo:[0,1,0]
	s_waitcnt lgkmcnt(0)
	v_pk_mul_f32 v[14:15], v[16:17], v[6:7] op_sel:[0,0] op_sel_hi:[0,1]
	v_pk_fma_f32 v[14:15], v[16:17], v[6:7], v[14:15] op_sel:[1,1,0] op_sel_hi:[1,0,1] neg_lo:[0,1,0]
	ds_write2_b64 v1, v[26:27], v[14:15] offset0:32 offset1:48
	v_pk_mul_f32 v[14:15], v[36:37], v[8:9] op_sel:[0,0] op_sel_hi:[0,1]
	v_pk_fma_f32 v[14:15], v[36:37], v[8:9], v[14:15] op_sel:[1,1,0] op_sel_hi:[1,0,1] neg_lo:[0,1,0]
	ds_read2_b64 v[2:5], v45 offset0:80 offset1:96
	s_waitcnt lgkmcnt(0)
	v_pk_mul_f32 v[16:17], v[34:35], v[2:3] op_sel:[0,0] op_sel_hi:[0,1]
	v_pk_fma_f32 v[16:17], v[34:35], v[2:3], v[16:17] op_sel:[1,1,0] op_sel_hi:[1,0,1] neg_lo:[0,1,0]
	ds_write2_b64 v1, v[14:15], v[16:17] offset0:64 offset1:80
	v_pk_mul_f32 v[14:15], v[18:19], v[4:5] op_sel:[0,0] op_sel_hi:[0,1]
	v_pk_fma_f32 v[14:15], v[18:19], v[4:5], v[14:15] op_sel:[1,1,0] op_sel_hi:[1,0,1] neg_lo:[0,1,0]
	ds_read2_b64 v[6:9], v45 offset0:112 offset1:128
	ds_read2_b64 v[2:5], v45 offset0:144 offset1:160
	s_waitcnt lgkmcnt(1)
	v_pk_mul_f32 v[16:17], v[38:39], v[6:7] op_sel:[0,0] op_sel_hi:[0,1]
	v_pk_fma_f32 v[16:17], v[38:39], v[6:7], v[16:17] op_sel:[1,1,0] op_sel_hi:[1,0,1] neg_lo:[0,1,0]
	ds_write2_b64 v1, v[14:15], v[16:17] offset0:96 offset1:112
	v_pk_mul_f32 v[14:15], v[30:31], v[8:9] op_sel:[0,0] op_sel_hi:[0,1]
	v_pk_fma_f32 v[14:15], v[30:31], v[8:9], v[14:15] op_sel:[1,1,0] op_sel_hi:[1,0,1] neg_lo:[0,1,0]
	ds_read2_b64 v[6:9], v45 offset0:176 offset1:192
	s_waitcnt lgkmcnt(2)
	v_pk_mul_f32 v[16:17], v[24:25], v[2:3] op_sel:[0,0] op_sel_hi:[0,1]
	v_pk_fma_f32 v[16:17], v[24:25], v[2:3], v[16:17] op_sel:[1,1,0] op_sel_hi:[1,0,1] neg_lo:[0,1,0]
	ds_write2_b64 v1, v[14:15], v[16:17] offset0:128 offset1:144
	v_pk_mul_f32 v[14:15], v[12:13], v[4:5] op_sel:[0,0] op_sel_hi:[0,1]
	v_pk_fma_f32 v[14:15], v[12:13], v[4:5], v[14:15] op_sel:[1,1,0] op_sel_hi:[1,0,1] neg_lo:[0,1,0]
	ds_read2_b64 v[2:5], v45 offset0:208 offset1:224
	s_waitcnt lgkmcnt(2)
	v_pk_mul_f32 v[12:13], v[28:29], v[6:7] op_sel:[0,0] op_sel_hi:[0,1]
	v_pk_fma_f32 v[12:13], v[28:29], v[6:7], v[12:13] op_sel:[1,1,0] op_sel_hi:[1,0,1] neg_lo:[0,1,0]
	ds_write2_b64 v1, v[32:33], v[42:43] offset1:16
	ds_write2_b64 v1, v[14:15], v[12:13] offset0:160 offset1:176
	ds_read_b64 v[6:7], v44 offset:36736
	v_pk_mul_f32 v[12:13], v[22:23], v[8:9] op_sel:[0,0] op_sel_hi:[0,1]
	v_pk_fma_f32 v[12:13], v[22:23], v[8:9], v[12:13] op_sel:[1,1,0] op_sel_hi:[1,0,1] neg_lo:[0,1,0]
	s_waitcnt lgkmcnt(3)
	v_pk_mul_f32 v[8:9], v[20:21], v[2:3] op_sel:[0,0] op_sel_hi:[0,1]
	v_pk_fma_f32 v[8:9], v[20:21], v[2:3], v[8:9] op_sel:[1,1,0] op_sel_hi:[1,0,1] neg_lo:[0,1,0]
	ds_write2_b64 v1, v[12:13], v[8:9] offset0:192 offset1:208
	v_pk_mul_f32 v[2:3], v[10:11], v[4:5] op_sel:[0,0] op_sel_hi:[0,1]
	v_pk_fma_f32 v[2:3], v[10:11], v[4:5], v[2:3] op_sel:[1,1,0] op_sel_hi:[1,0,1] neg_lo:[0,1,0]
	s_waitcnt lgkmcnt(1)
	v_pk_mul_f32 v[4:5], v[40:41], v[6:7] op_sel:[0,0] op_sel_hi:[0,1]
	v_pk_fma_f32 v[4:5], v[40:41], v[6:7], v[4:5] op_sel:[1,1,0] op_sel_hi:[1,0,1] neg_lo:[0,1,0]
	ds_write2_b64 v1, v[2:3], v[4:5] offset0:224 offset1:240
	v_mov_b32_e32 v1, v0
	s_waitcnt lgkmcnt(0)
	s_barrier
	v_mov_b32_e32 v53, 0
	v_and_b32_e32 v2, 15, v1
	v_and_b32_e32 v1, 0x1ffffff0, v1
	v_lshlrev_b32_e32 v1, 3, v1
	v_mad_u32_u24 v1, v2, s5, v1
	ds_read2_b64 v[2:5], v1 offset1:1
	ds_read2_b64 v[6:9], v1 offset0:2 offset1:3
	ds_read2_b64 v[10:13], v1 offset0:8 offset1:9
	ds_read2_b64 v[18:21], v1 offset0:4 offset1:5
	ds_read2_b64 v[22:25], v1 offset0:6 offset1:7
	ds_read2_b64 v[26:29], v1 offset0:12 offset1:13
	ds_read2_b64 v[30:33], v1 offset0:10 offset1:11
	ds_read2_b64 v[34:37], v1 offset0:14 offset1:15
	s_waitcnt lgkmcnt(5)
	v_pk_add_f32 v[14:15], v[2:3], v[10:11]
	v_pk_add_f32 v[2:3], v[2:3], v[10:11] neg_lo:[0,1] neg_hi:[0,1]
	s_waitcnt lgkmcnt(2)
	v_pk_add_f32 v[10:11], v[18:19], v[26:27]
	v_pk_add_f32 v[18:19], v[18:19], v[26:27] neg_lo:[0,1] neg_hi:[0,1]
	v_pk_add_f32 v[26:27], v[14:15], v[10:11]
	v_pk_add_f32 v[16:17], v[14:15], v[10:11] neg_lo:[0,1] neg_hi:[0,1]
	v_pk_add_f32 v[14:15], v[2:3], v[18:19] op_sel:[0,1] op_sel_hi:[1,0] neg_hi:[0,1]
	v_pk_add_f32 v[18:19], v[2:3], v[18:19] op_sel:[0,1] op_sel_hi:[1,0] neg_lo:[0,1]
	v_pk_add_f32 v[2:3], v[4:5], v[12:13]
	v_pk_add_f32 v[10:11], v[20:21], v[28:29]
	v_pk_add_f32 v[4:5], v[4:5], v[12:13] neg_lo:[0,1] neg_hi:[0,1]
	v_pk_add_f32 v[12:13], v[20:21], v[28:29] neg_lo:[0,1] neg_hi:[0,1]
	v_pk_add_f32 v[28:29], v[2:3], v[10:11]
	v_pk_add_f32 v[2:3], v[2:3], v[10:11] neg_lo:[0,1] neg_hi:[0,1]
	v_pk_add_f32 v[10:11], v[4:5], v[12:13] op_sel:[0,1] op_sel_hi:[1,0] neg_hi:[0,1]
	v_pk_add_f32 v[4:5], v[4:5], v[12:13] op_sel:[0,1] op_sel_hi:[1,0] neg_lo:[0,1]
	s_waitcnt lgkmcnt(1)
	v_pk_add_f32 v[12:13], v[6:7], v[30:31]
	s_waitcnt lgkmcnt(0)
	v_pk_add_f32 v[20:21], v[22:23], v[34:35]
	v_pk_add_f32 v[2:3], v[2:3], v[2:3] op_sel:[0,1] op_sel_hi:[1,0] neg_hi:[0,1]
	v_pk_add_f32 v[6:7], v[6:7], v[30:31] neg_lo:[0,1] neg_hi:[0,1]
	v_pk_add_f32 v[22:23], v[22:23], v[34:35] neg_lo:[0,1] neg_hi:[0,1]
	v_pk_add_f32 v[30:31], v[12:13], v[20:21]
	v_pk_add_f32 v[20:21], v[12:13], v[20:21] neg_lo:[0,1] neg_hi:[0,1]
	v_pk_add_f32 v[12:13], v[6:7], v[22:23] op_sel:[0,1] op_sel_hi:[1,0] neg_hi:[0,1]
	v_pk_mul_f32 v[44:45], v[2:3], s[8:9]
	v_pk_add_f32 v[6:7], v[6:7], v[22:23] op_sel:[0,1] op_sel_hi:[1,0] neg_lo:[0,1]
	v_pk_add_f32 v[22:23], v[8:9], v[32:33]
	v_pk_add_f32 v[2:3], v[12:13], v[12:13] op_sel:[0,1] op_sel_hi:[1,0] neg_hi:[0,1]
	v_pk_add_f32 v[8:9], v[8:9], v[32:33] neg_lo:[0,1] neg_hi:[0,1]
	v_pk_add_f32 v[32:33], v[24:25], v[36:37]
	v_pk_mul_f32 v[12:13], v[2:3], s[8:9]
	v_pk_add_f32 v[2:3], v[6:7], v[6:7] op_sel:[0,1] op_sel_hi:[1,0] neg_lo:[0,1]
	v_pk_add_f32 v[24:25], v[24:25], v[36:37] neg_lo:[0,1] neg_hi:[0,1]
	v_pk_add_f32 v[34:35], v[22:23], v[32:33]
	v_pk_add_f32 v[32:33], v[22:23], v[32:33] neg_lo:[0,1] neg_hi:[0,1]
	v_pk_mul_f32 v[54:55], v[2:3], s[12:13]
	v_pk_add_f32 v[36:37], v[8:9], v[24:25] op_sel:[0,1] op_sel_hi:[1,0] neg_hi:[0,1]
	v_pk_add_f32 v[8:9], v[8:9], v[24:25] op_sel:[0,1] op_sel_hi:[1,0] neg_lo:[0,1]
	v_pk_mul_f32 v[22:23], v[4:5], s[10:11] op_sel:[0,0] op_sel_hi:[0,1]
	v_pk_fma_f32 v[22:23], v[4:5], s[10:11], v[22:23] op_sel:[1,1,0] op_sel_hi:[1,0,1] neg_lo:[0,1,0]
	v_pk_add_f32 v[4:5], v[28:29], v[34:35]
	v_pk_add_f32 v[2:3], v[32:33], v[32:33] op_sel:[0,1] op_sel_hi:[1,0] neg_lo:[0,1]
	v_pk_add_f32 v[28:29], v[28:29], v[34:35] neg_lo:[0,1] neg_hi:[0,1]
	v_pk_mul_f32 v[32:33], v[2:3], s[12:13]
	v_pk_add_f32 v[2:3], v[26:27], v[30:31]
	v_pk_add_f32 v[26:27], v[26:27], v[30:31] neg_lo:[0,1] neg_hi:[0,1]
	v_pk_mul_f32 v[24:25], v[10:11], s[6:7] op_sel:[0,0] op_sel_hi:[0,1]
	v_pk_fma_f32 v[24:25], v[10:11], s[6:7], v[24:25] op_sel:[1,1,0] op_sel_hi:[1,0,1] neg_lo:[0,1,0]
	v_pk_mul_f32 v[6:7], v[36:37], s[10:11] op_sel:[0,0] op_sel_hi:[0,1]
	v_pk_fma_f32 v[6:7], v[36:37], s[10:11], v[6:7] op_sel:[1,1,0] op_sel_hi:[1,0,1] neg_lo:[0,1,0]
	v_pk_mul_f32 v[56:57], v[8:9], s[14:15] op_sel:[0,0] op_sel_hi:[0,1]
	v_pk_fma_f32 v[56:57], v[8:9], s[14:15], v[56:57] op_sel:[1,1,0] op_sel_hi:[1,0,1] neg_lo:[0,1,0]
	v_pk_add_f32 v[10:11], v[2:3], v[4:5]
	v_lshlrev_b32_e32 v34, 2, v0
	v_pk_add_f32 v[4:5], v[2:3], v[4:5] neg_lo:[0,1] neg_hi:[0,1]
	v_pk_add_f32 v[8:9], v[26:27], v[28:29] op_sel:[0,1] op_sel_hi:[1,0] neg_hi:[0,1]
	v_pk_add_f32 v[2:3], v[26:27], v[28:29] op_sel:[0,1] op_sel_hi:[1,0] neg_lo:[0,1]
	v_pk_add_f32 v[26:27], v[14:15], v[12:13]
	v_pk_add_f32 v[28:29], v[24:25], v[6:7]
	v_add_u32_e32 v1, 0x400, v34
	v_pk_add_f32 v[14:15], v[14:15], v[12:13] neg_lo:[0,1] neg_hi:[0,1]
	v_pk_add_f32 v[30:31], v[24:25], v[6:7] neg_lo:[0,1] neg_hi:[0,1]
	v_pk_add_f32 v[12:13], v[26:27], v[28:29]
	v_pk_add_f32 v[6:7], v[26:27], v[28:29] neg_lo:[0,1] neg_hi:[0,1]
	v_add_u32_e32 v24, 0x800, v34
	v_add_u32_e32 v25, 0xc00, v34
	v_add_u32_e32 v26, 0x1000, v34
	v_add_u32_e32 v27, 0x1400, v34
	v_add_u32_e32 v28, 0x1800, v34
	v_add_u32_e32 v29, 0x1c00, v34
	v_add_u32_e32 v35, 0x2000, v34
	s_waitcnt vmcnt(0)
	v_mov_b32_e32 v1, v113
	s_nop 0
	v_mov_b32_e32 v36, v114
	v_mov_b32_e32 v37, v115
	v_mov_b32_e32 v38, v116
	v_mov_b32_e32 v39, v117
	v_mov_b32_e32 v40, v118
	v_mov_b32_e32 v41, v119
	v_mov_b32_e32 v42, v120
	v_add_u32_e32 v24, 0x2400, v34
	v_add_u32_e32 v25, 0x2800, v34
	v_add_u32_e32 v26, 0x2c00, v34
	v_add_u32_e32 v27, 0x3000, v34
	v_add_u32_e32 v28, 0x3400, v34
	v_add_u32_e32 v35, 0x3800, v34
	v_mov_b32_e32 v52, v112
	v_mov_b32_e32 v43, v126
	v_add_u32_e32 v29, 0x3c00, v34
	v_mov_b32_e32 v47, v121
	v_mov_b32_e32 v48, v122
	v_mov_b32_e32 v49, v123
	v_mov_b32_e32 v50, v124
	v_mov_b32_e32 v51, v125
	v_mov_b32_e32 v46, v127
	v_pk_add_f32 v[26:27], v[16:17], v[20:21] op_sel:[0,1] op_sel_hi:[1,0] neg_hi:[0,1]
	v_pk_add_f32 v[16:17], v[16:17], v[20:21] op_sel:[0,1] op_sel_hi:[1,0] neg_lo:[0,1]
	v_pk_add_f32 v[20:21], v[44:45], v[32:33]
	v_pk_add_f32 v[28:29], v[44:45], v[32:33] neg_lo:[0,1] neg_hi:[0,1]
	v_pk_add_f32 v[24:25], v[14:15], v[30:31] op_sel:[0,1] op_sel_hi:[1,0] neg_hi:[0,1]
	v_pk_add_f32 v[14:15], v[14:15], v[30:31] op_sel:[0,1] op_sel_hi:[1,0] neg_lo:[0,1]
	v_pk_add_f32 v[30:31], v[20:21], v[26:27]
	v_pk_add_f32 v[20:21], v[26:27], v[20:21] neg_lo:[0,1] neg_hi:[0,1]
	v_pk_add_f32 v[26:27], v[16:17], v[28:29] op_sel:[0,1] op_sel_hi:[1,0] neg_hi:[0,1]
	v_pk_add_f32 v[16:17], v[16:17], v[28:29] op_sel:[0,1] op_sel_hi:[1,0] neg_lo:[0,1]
	v_pk_add_f32 v[28:29], v[18:19], v[54:55]
	v_pk_add_f32 v[44:45], v[22:23], v[56:57]
	s_mov_b32 s2, 0xff61b1e6
	v_pk_add_f32 v[18:19], v[18:19], v[54:55] neg_lo:[0,1] neg_hi:[0,1]
	v_pk_add_f32 v[54:55], v[22:23], v[56:57] neg_lo:[0,1] neg_hi:[0,1]
	v_pk_add_f32 v[32:33], v[28:29], v[44:45]
	v_pk_add_f32 v[22:23], v[28:29], v[44:45] neg_lo:[0,1] neg_hi:[0,1]
	v_max3_f32 v44, v10, s2, v12
	v_max3_f32 v44, v44, v30, v32
	v_max3_f32 v44, v44, v8, v24
	v_pk_add_f32 v[28:29], v[18:19], v[54:55] op_sel:[0,1] op_sel_hi:[1,0] neg_hi:[0,1]
	v_pk_add_f32 v[18:19], v[18:19], v[54:55] op_sel:[0,1] op_sel_hi:[1,0] neg_lo:[0,1]
	v_max3_f32 v45, -v11, s2, -v13
	v_max3_f32 v44, v44, v26, v28
	v_max3_f32 v44, v44, v4, v6
	v_max3_f32 v44, v44, v20, v22
	v_max3_f32 v44, v44, v2, v14
	v_max3_f32 v44, v44, v16, v18
	v_max3_f32 v45, v45, -v31, -v33
	v_max3_f32 v45, v45, -v9, -v25
	v_mov_b32_dpp v53, v44 quad_perm:[1,0,3,2] row_mask:0xf bank_mask:0xf
	v_max_f32_e32 v53, v53, v53
	v_max_f32_e32 v44, v44, v53
	v_mov_b32_e32 v53, 0
	v_max3_f32 v45, v45, -v27, -v29
	v_max3_f32 v45, v45, -v5, -v7
	v_mov_b32_dpp v53, v44 quad_perm:[2,3,0,1] row_mask:0xf bank_mask:0xf
	v_max_f32_e32 v53, v53, v53
	v_max_f32_e32 v44, v44, v53
	v_mov_b32_e32 v53, 0
	v_max3_f32 v45, v45, -v21, -v23
	v_max3_f32 v45, v45, -v3, -v15
	v_mov_b32_dpp v53, v44 row_half_mirror row_mask:0xf bank_mask:0xf
	v_max_f32_e32 v53, v53, v53
	v_max_f32_e32 v44, v44, v53
	v_mov_b32_e32 v53, 0
	v_max3_f32 v45, v45, -v17, -v19
	s_nop 0
	v_mov_b32_dpp v53, v44 row_mirror row_mask:0xf bank_mask:0xf
	v_max_f32_e32 v53, v53, v53
	v_max_f32_e32 v44, v44, v53
	s_nop 0
	v_readlane_b32 s5, v44, 0
	v_readlane_b32 s6, v44, 16
	v_readlane_b32 s7, v44, 32
	v_readlane_b32 s8, v44, 48
	v_mov_b32_e32 v44, 0
	s_nop 1
	v_mov_b32_dpp v44, v45 quad_perm:[1,0,3,2] row_mask:0xf bank_mask:0xf
	v_max_f32_e32 v44, v44, v44
	v_max_f32_e32 v44, v45, v44
	v_mov_b32_e32 v45, 0
	s_nop 1
	v_mov_b32_dpp v45, v44 quad_perm:[2,3,0,1] row_mask:0xf bank_mask:0xf
	v_max_f32_e32 v45, v45, v45
	v_max_f32_e32 v44, v44, v45
	v_mov_b32_e32 v45, 0
	s_nop 1
	v_mov_b32_dpp v45, v44 row_half_mirror row_mask:0xf bank_mask:0xf
	v_max_f32_e32 v45, v45, v45
	v_max_f32_e32 v44, v44, v45
	v_mov_b32_e32 v45, 0
	s_nop 1
	v_mov_b32_dpp v45, v44 row_mirror row_mask:0xf bank_mask:0xf
	v_max_f32_e32 v45, v45, v45
	v_max_f32_e32 v44, v44, v45
	v_and_b32_e32 v45, 63, v0
	v_readlane_b32 s9, v44, 0
	v_readlane_b32 s10, v44, 16
	v_readlane_b32 s11, v44, 32
	v_readlane_b32 s12, v44, 48
	v_ashrrev_i32_e32 v44, 6, v0
	v_cmp_eq_u32_e32 vcc, 0, v45
	v_lshlrev_b32_e32 v61, 3, v44
	s_and_saveexec_b64 s[2:3], vcc
	s_cbranch_execz .LBB1_10
	v_max_f32_e64 v44, s12, s12
	v_max_f32_e64 v45, s11, s11
	v_max_f32_e32 v44, v45, v44
	v_mov_b32_e32 v45, s10
	v_max3_f32 v45, s9, v45, v44
	v_max_f32_e64 v44, s8, s8
	v_max_f32_e64 v53, s7, s7
	v_max_f32_e32 v44, v53, v44
	v_mov_b32_e32 v53, s6
	v_max3_f32 v44, s5, v53, v44
	ds_write_b64 v61, v[44:45] offset:36864
